# baseline (speedup 1.0000x reference)
_Z16bilateral_kernelPKfS0_Pf:
	s_load_dwordx2 s[4:5], s[0:1], 0x0
	s_load_dwordx2 s[8:9], s[0:1], 0x10
	s_and_b32 s0, s2, 7
	s_mulk_i32 s0, 0x60
	s_lshr_b32 s1, s2, 3
	s_add_i32 s1, s0, s1
	s_lshr_b32 s0, s1, 6
	s_lshl_b32 s11, s1, 6
	s_and_b32 s11, s11, 0x1c0
	s_lshl_b32 s1, s1, 3
	s_nop 0
	s_and_b32 s10, s1, 0x1c0
	s_mov_b32 s1, 0
	s_lshl_b64 s[2:3], s[0:1], 20
	s_mov_b32 s20, 0xc05dfbe6
	s_mov_b32 s21, 0xc05dfbe6
	s_mov_b32 s22, 0xc0a8390e
	s_mov_b32 s23, 0xc0a8390e
	s_mov_b32 s24, 0xc08211a7
	s_mov_b32 s25, 0xc08211a7
	s_mov_b32 s26, 0xc0bb4cc1
	s_mov_b32 s27, 0xc0bb4cc1
	s_mov_b32 s28, 0xc0f487dc
	s_mov_b32 s29, 0xc0f487dc
	s_mov_b32 s30, 0x3e0bd796
	s_mov_b32 s31, 0x3e0bd796
	s_mov_b32 s32, 0x3f45a90c
	s_mov_b32 s33, 0x3f45a90c
	s_mov_b32 s34, 0x3fa5c782
	s_mov_b32 s35, 0x3fa5c782
	v_and_b32_e32 v118, 15, v0
	v_lshrrev_b32_e32 v115, 2, v0
	v_lshl_or_b32 v113, v118, 2, s11
	v_and_or_b32 v117, v115, 60, s10
	v_min_u32_e32 v116, 0x1fa, v113
	v_sub_u32_e64 v115, v113, 2 clamp
	v_add_u32_e64 v116, 4, v116
	v_cmp_eq_u32_e64 s[16:17], 0, v118
	v_cmp_eq_u32_e32 vcc, 15, v118
	s_nop 1
	v_cndmask_b32_e64 v115, v116, v115, s[16:17]
	s_or_b64 vcc, s[16:17], vcc
	v_lshlrev_b32_e32 v115, 2, v115
	v_mov_b32_e32 v116, 0x7ff00000
	s_nop 0
	v_cndmask_b32_e32 v112, v116, v115, vcc
	s_movk_i32 s18, 0x1fc
	v_cmp_eq_u32_e32 vcc, 0, v113
	v_cmp_eq_u32_e64 s[16:17], s18, v113
	v_lshlrev_b32_e32 v113, 2, v113
	s_waitcnt lgkmcnt(0)
	s_add_u32 s4, s4, s2
	s_addc_u32 s5, s5, s3
	s_and_b32 s5, s5, 0xffff
	s_mov_b32 s6, 0x100000
	s_mov_b32 s7, 0x20000
	s_add_u32 s12, s8, s2
	s_addc_u32 s13, s9, s3
	s_and_b32 s13, s13, 0xffff
	s_mov_b32 s14, 0x100000
	s_mov_b32 s15, 0x20000
	v_sub_u32_e64 v115, v117, 2 clamp
	v_lshlrev_b32_e32 v115, 11, v115
	v_add_u32_e32 v116, v115, v112
	v_add_u32_e64 v115, v115, v113
	buffer_load_dwordx2 v[0:1], v116, s[4:7], 0 offen nt
	buffer_load_dwordx2 v[6:7], v116, s[4:7], 0 offen nt
	buffer_load_dwordx4 v[2:5], v115, s[4:7], 0 offen nt
	v_sub_u32_e64 v115, v117, 1 clamp
	v_lshlrev_b32_e32 v115, 11, v115
	v_add_u32_e32 v116, v115, v112
	v_add_u32_e64 v115, v115, v113
	buffer_load_dwordx2 v[8:9], v116, s[4:7], 0 offen nt
	buffer_load_dwordx2 v[14:15], v116, s[4:7], 0 offen nt
	buffer_load_dwordx4 v[10:13], v115, s[4:7], 0 offen nt
	v_lshlrev_b32_e32 v115, 11, v117
	v_add_u32_e32 v116, v115, v112
	v_add_u32_e64 v114, v115, v113
	v_add_u32_e32 v119, 0x1000, v114
	buffer_load_dwordx2 v[16:17], v116, s[4:7], 0 offen nt
	buffer_load_dwordx2 v[22:23], v116, s[4:7], 0 offen nt
	buffer_load_dwordx4 v[18:21], v114, s[4:7], 0 offen nt
	v_lshlrev_b32_e64 v115, 11, v117
	v_add_u32_e32 v115, 0x800, v115
	v_add_u32_e32 v116, v115, v112
	v_add_u32_e32 v115, v115, v113
	buffer_load_dwordx2 v[24:25], v116, s[4:7], 0 offen nt
	buffer_load_dwordx2 v[30:31], v116, s[4:7], 0 offen nt
	buffer_load_dwordx4 v[26:29], v115, s[4:7], 0 offen nt
	v_lshlrev_b32_e64 v115, 11, v117
	v_add_u32_e32 v115, 0x1000, v115
	v_add_u32_e32 v116, v115, v112
	v_add_u32_e32 v115, v115, v113
	buffer_load_dwordx2 v[32:33], v116, s[4:7], 0 offen nt
	buffer_load_dwordx2 v[38:39], v116, s[4:7], 0 offen nt
	buffer_load_dwordx4 v[34:37], v115, s[4:7], 0 offen nt
	v_lshlrev_b32_e64 v115, 11, v117
	v_add_u32_e32 v115, 0x1800, v115
	v_add_u32_e32 v116, v115, v112
	v_add_u32_e32 v115, v115, v113
	buffer_load_dwordx2 v[40:41], v116, s[4:7], 0 offen nt
	buffer_load_dwordx2 v[46:47], v116, s[4:7], 0 offen nt
	buffer_load_dwordx4 v[42:45], v115, s[4:7], 0 offen nt
	v_min_u32_e32 v115, 0x1fb, v117
	v_lshlrev_b32_e64 v115, 11, v115
	v_add_u32_e32 v115, 0x2000, v115
	v_add_u32_e32 v116, v115, v112
	v_add_u32_e32 v115, v115, v113
	buffer_load_dwordx2 v[48:49], v116, s[4:7], 0 offen nt
	buffer_load_dwordx2 v[54:55], v116, s[4:7], 0 offen nt
	buffer_load_dwordx4 v[50:53], v115, s[4:7], 0 offen nt
	v_min_u32_e32 v115, 0x1fa, v117
	v_lshlrev_b32_e64 v115, 11, v115
	v_add_u32_e32 v115, 0x2800, v115
	v_add_u32_e32 v116, v115, v112
	v_add_u32_e32 v115, v115, v113
	buffer_load_dwordx2 v[56:57], v116, s[4:7], 0 offen nt
	buffer_load_dwordx2 v[62:63], v116, s[4:7], 0 offen nt
	buffer_load_dwordx4 v[58:61], v115, s[4:7], 0 offen nt
	s_waitcnt vmcnt(21)
	s_nop 0
	v_mov_b32_dpp v0, v4 row_shr:1 row_mask:0xf bank_mask:0xf
	v_mov_b32_dpp v1, v5 row_shr:1 row_mask:0xf bank_mask:0xf
	v_mov_b32_dpp v6, v2 row_shl:1 row_mask:0xf bank_mask:0xf
	v_mov_b32_dpp v7, v3 row_shl:1 row_mask:0xf bank_mask:0xf
	v_pk_mul_f32 v[2:3], v[2:3], s[32:33]
	v_pk_mul_f32 v[4:5], v[4:5], s[32:33]
	v_cndmask_b32_e64 v1, v1, v0, vcc
	v_cndmask_b32_e64 v6, v6, v7, s[16:17]
	v_pk_mul_f32 v[0:1], v[0:1], s[32:33]
	v_pk_mul_f32 v[6:7], v[6:7], s[32:33]
	s_waitcnt vmcnt(18)
	s_nop 0
	v_mov_b32_dpp v8, v12 row_shr:1 row_mask:0xf bank_mask:0xf
	v_mov_b32_dpp v9, v13 row_shr:1 row_mask:0xf bank_mask:0xf
	v_mov_b32_dpp v14, v10 row_shl:1 row_mask:0xf bank_mask:0xf
	v_mov_b32_dpp v15, v11 row_shl:1 row_mask:0xf bank_mask:0xf
	v_pk_mul_f32 v[10:11], v[10:11], s[32:33]
	v_pk_mul_f32 v[12:13], v[12:13], s[32:33]
	v_cndmask_b32_e64 v9, v9, v8, vcc
	v_cndmask_b32_e64 v14, v14, v15, s[16:17]
	v_pk_mul_f32 v[8:9], v[8:9], s[32:33]
	v_pk_mul_f32 v[14:15], v[14:15], s[32:33]
	s_waitcnt vmcnt(15)
	s_nop 0
	v_mov_b32_dpp v16, v20 row_shr:1 row_mask:0xf bank_mask:0xf
	v_mov_b32_dpp v17, v21 row_shr:1 row_mask:0xf bank_mask:0xf
	v_mov_b32_dpp v22, v18 row_shl:1 row_mask:0xf bank_mask:0xf
	v_mov_b32_dpp v23, v19 row_shl:1 row_mask:0xf bank_mask:0xf
	v_pk_mul_f32 v[18:19], v[18:19], s[32:33]
	v_pk_mul_f32 v[20:21], v[20:21], s[32:33]
	v_cndmask_b32_e64 v17, v17, v16, vcc
	v_cndmask_b32_e64 v22, v22, v23, s[16:17]
	v_pk_mul_f32 v[68:69], v[18:19], s[30:31]
	v_pk_mul_f32 v[70:71], v[20:21], s[30:31]
	v_pk_mul_f32 v[16:17], v[16:17], s[32:33]
	v_pk_mul_f32 v[22:23], v[22:23], s[32:33]
	v_mov_b32_e32 v64, s30
	v_mov_b32_e32 v65, s30
	v_mov_b32_e64 v66, s30
	v_mov_b32_e32 v67, s30
	s_setprio 3
	v_pk_add_f32 v[96:97], v[18:19], v[0:1] neg_lo:[0,1] neg_hi:[0,1]
	v_pk_add_f32 v[98:99], v[18:19], v[2:3] neg_lo:[0,1] neg_hi:[0,1]
	v_pk_add_f32 v[100:101], v[20:21], v[2:3] neg_lo:[0,1] neg_hi:[0,1]
	v_pk_add_f32 v[102:103], v[18:19], v[4:5] neg_lo:[0,1] neg_hi:[0,1]
	v_pk_fma_f32 v[96:97], v[96:97], v[96:97], s[28:29] neg_lo:[1,0,0] neg_hi:[1,0,0]
	v_pk_fma_f32 v[98:99], v[98:99], v[98:99], s[22:23] neg_lo:[1,0,0] neg_hi:[1,0,0]
	v_pk_fma_f32 v[100:101], v[100:101], v[100:101], s[28:29] neg_lo:[1,0,0] neg_hi:[1,0,0]
	v_pk_fma_f32 v[102:103], v[102:103], v[102:103], s[28:29] neg_lo:[1,0,0] neg_hi:[1,0,0]
	v_exp_f32_e32 v96, v96
	v_exp_f32_e32 v97, v97
	v_exp_f32_e32 v98, v98
	v_exp_f32_e32 v99, v99
	v_exp_f32_e32 v100, v100
	v_exp_f32_e32 v101, v101
	v_exp_f32_e32 v102, v102
	v_exp_f32_e32 v103, v103
	v_pk_add_f32 v[104:105], v[20:21], v[4:5] neg_lo:[0,1] neg_hi:[0,1]
	v_pk_add_f32 v[106:107], v[20:21], v[6:7] neg_lo:[0,1] neg_hi:[0,1]
	v_pk_add_f32 v[108:109], v[18:19], v[2:3] op_sel:[1,0] op_sel_hi:[0,1] neg_lo:[0,1] neg_hi:[0,1]
	v_pk_add_f32 v[110:111], v[20:21], v[4:5] op_sel:[1,0] op_sel_hi:[0,1] neg_lo:[0,1] neg_hi:[0,1]
	v_pk_fma_f32 v[104:105], v[104:105], v[104:105], s[22:23] neg_lo:[1,0,0] neg_hi:[1,0,0]
	v_pk_fma_f32 v[106:107], v[106:107], v[106:107], s[28:29] neg_lo:[1,0,0] neg_hi:[1,0,0]
	v_pk_fma_f32 v[108:109], v[108:109], v[108:109], s[26:27] neg_lo:[1,0,0] neg_hi:[1,0,0]
	v_pk_fma_f32 v[110:111], v[110:111], v[110:111], s[26:27] neg_lo:[1,0,0] neg_hi:[1,0,0]
	v_exp_f32_e32 v104, v104
	v_exp_f32_e32 v105, v105
	v_exp_f32_e32 v106, v106
	v_exp_f32_e32 v107, v107
	v_exp_f32_e32 v108, v108
	v_exp_f32_e32 v109, v109
	v_exp_f32_e32 v110, v110
	v_exp_f32_e32 v111, v111
	v_pk_add_f32 v[64:65], v[64:65], v[96:97]
	v_pk_fma_f32 v[68:69], v[96:97], v[0:1], v[68:69]
	v_pk_add_f32 v[66:67], v[66:67], v[100:101]
	v_pk_add_f32 v[64:65], v[64:65], v[98:99]
	v_pk_fma_f32 v[68:69], v[98:99], v[2:3], v[68:69]
	v_pk_fma_f32 v[70:71], v[100:101], v[2:3], v[70:71]
	v_pk_add_f32 v[64:65], v[64:65], v[102:103]
	v_pk_fma_f32 v[68:69], v[102:103], v[4:5], v[68:69]
	v_pk_add_f32 v[96:97], v[18:19], v[8:9] neg_lo:[0,1] neg_hi:[0,1]
	v_pk_add_f32 v[98:99], v[18:19], v[10:11] neg_lo:[0,1] neg_hi:[0,1]
	v_pk_add_f32 v[100:101], v[20:21], v[10:11] neg_lo:[0,1] neg_hi:[0,1]
	v_pk_add_f32 v[102:103], v[18:19], v[12:13] neg_lo:[0,1] neg_hi:[0,1]
	v_pk_fma_f32 v[96:97], v[96:97], v[96:97], s[26:27] neg_lo:[1,0,0] neg_hi:[1,0,0]
	v_pk_fma_f32 v[98:99], v[98:99], v[98:99], s[20:21] neg_lo:[1,0,0] neg_hi:[1,0,0]
	v_pk_fma_f32 v[100:101], v[100:101], v[100:101], s[26:27] neg_lo:[1,0,0] neg_hi:[1,0,0]
	v_pk_fma_f32 v[102:103], v[102:103], v[102:103], s[26:27] neg_lo:[1,0,0] neg_hi:[1,0,0]
	v_exp_f32_e32 v96, v96
	v_exp_f32_e32 v97, v97
	v_exp_f32_e32 v98, v98
	v_exp_f32_e32 v99, v99
	v_exp_f32_e32 v100, v100
	v_exp_f32_e32 v101, v101
	v_exp_f32_e32 v102, v102
	v_exp_f32_e32 v103, v103
	v_pk_add_f32 v[66:67], v[66:67], v[104:105]
	v_pk_fma_f32 v[70:71], v[104:105], v[4:5], v[70:71]
	v_pk_add_f32 v[64:65], v[64:65], v[108:109] op_sel:[0,1] op_sel_hi:[1,0]
	v_pk_add_f32 v[66:67], v[66:67], v[106:107]
	v_pk_fma_f32 v[70:71], v[106:107], v[6:7], v[70:71]
	v_pk_fma_f32 v[68:69], v[108:109], v[2:3], v[68:69] op_sel:[1,1,0] op_sel_hi:[0,0,1]
	v_pk_add_f32 v[66:67], v[66:67], v[110:111] op_sel:[0,1] op_sel_hi:[1,0]
	v_pk_fma_f32 v[70:71], v[110:111], v[4:5], v[70:71] op_sel:[1,1,0] op_sel_hi:[0,0,1]
	v_pk_add_f32 v[104:105], v[20:21], v[12:13] neg_lo:[0,1] neg_hi:[0,1]
	v_pk_add_f32 v[106:107], v[20:21], v[14:15] neg_lo:[0,1] neg_hi:[0,1]
	v_pk_add_f32 v[108:109], v[18:19], v[10:11] op_sel:[1,0] op_sel_hi:[0,1] neg_lo:[0,1] neg_hi:[0,1]
	v_pk_add_f32 v[110:111], v[20:21], v[12:13] op_sel:[1,0] op_sel_hi:[0,1] neg_lo:[0,1] neg_hi:[0,1]
	v_pk_fma_f32 v[104:105], v[104:105], v[104:105], s[20:21] neg_lo:[1,0,0] neg_hi:[1,0,0]
	v_pk_fma_f32 v[106:107], v[106:107], v[106:107], s[26:27] neg_lo:[1,0,0] neg_hi:[1,0,0]
	v_pk_fma_f32 v[108:109], v[108:109], v[108:109], s[24:25] neg_lo:[1,0,0] neg_hi:[1,0,0]
	v_pk_fma_f32 v[110:111], v[110:111], v[110:111], s[24:25] neg_lo:[1,0,0] neg_hi:[1,0,0]
	v_exp_f32_e32 v104, v104
	v_exp_f32_e32 v105, v105
	v_exp_f32_e32 v106, v106
	v_exp_f32_e32 v107, v107
	v_exp_f32_e32 v108, v108
	v_exp_f32_e32 v109, v109
	v_exp_f32_e32 v110, v110
	v_exp_f32_e32 v111, v111
	v_pk_add_f32 v[64:65], v[64:65], v[96:97]
	v_pk_fma_f32 v[68:69], v[96:97], v[8:9], v[68:69]
	v_pk_add_f32 v[66:67], v[66:67], v[100:101]
	v_pk_add_f32 v[64:65], v[64:65], v[98:99]
	v_pk_fma_f32 v[68:69], v[98:99], v[10:11], v[68:69]
	v_pk_fma_f32 v[70:71], v[100:101], v[10:11], v[70:71]
	v_pk_add_f32 v[64:65], v[64:65], v[102:103]
	v_pk_fma_f32 v[68:69], v[102:103], v[12:13], v[68:69]
	v_pk_add_f32 v[96:97], v[18:19], v[16:17] neg_lo:[0,1] neg_hi:[0,1]
	v_pk_add_f32 v[98:99], v[20:21], v[18:19] neg_lo:[0,1] neg_hi:[0,1]
	v_pk_add_f32 v[100:101], v[22:23], v[20:21] neg_lo:[0,1] neg_hi:[0,1]
	v_pk_fma_f32 v[96:97], v[96:97], v[96:97], s[22:23] neg_lo:[1,0,0] neg_hi:[1,0,0]
	v_pk_fma_f32 v[98:99], v[98:99], v[98:99], s[22:23] neg_lo:[1,0,0] neg_hi:[1,0,0]
	v_pk_fma_f32 v[100:101], v[100:101], v[100:101], s[22:23] neg_lo:[1,0,0] neg_hi:[1,0,0]
	v_exp_f32_e32 v96, v96
	v_exp_f32_e32 v97, v97
	v_exp_f32_e32 v98, v98
	v_exp_f32_e32 v99, v99
	v_exp_f32_e32 v100, v100
	v_exp_f32_e32 v101, v101
	v_pk_add_f32 v[66:67], v[66:67], v[104:105]
	v_pk_fma_f32 v[70:71], v[104:105], v[12:13], v[70:71]
	v_pk_add_f32 v[64:65], v[64:65], v[108:109] op_sel:[0,1] op_sel_hi:[1,0]
	v_pk_add_f32 v[66:67], v[66:67], v[106:107]
	v_pk_fma_f32 v[70:71], v[106:107], v[14:15], v[70:71]
	v_pk_fma_f32 v[68:69], v[108:109], v[10:11], v[68:69] op_sel:[1,1,0] op_sel_hi:[0,0,1]
	v_pk_add_f32 v[66:67], v[66:67], v[110:111] op_sel:[0,1] op_sel_hi:[1,0]
	v_pk_fma_f32 v[70:71], v[110:111], v[12:13], v[70:71] op_sel:[1,1,0] op_sel_hi:[0,0,1]
	v_sub_f32_e32 v104, v18, v1
	v_sub_f32_e32 v106, v20, v3
	v_sub_f32_e32 v108, v19, v4
	v_sub_f32_e32 v110, v21, v6
	v_sub_f32_e32 v105, v18, v9
	v_sub_f32_e32 v107, v20, v11
	v_sub_f32_e32 v109, v19, v12
	v_sub_f32_e32 v111, v21, v14
	v_fma_f32 v104, -v104, v104, s26
	v_fma_f32 v106, -v106, v106, s26
	v_fma_f32 v108, -v108, v108, s26
	v_fma_f32 v110, -v110, v110, s26
	v_fma_f32 v105, -v105, v105, s24
	v_fma_f32 v107, -v107, v107, s24
	v_fma_f32 v109, -v109, v109, s24
	v_fma_f32 v111, -v111, v111, s24
	v_exp_f32_e32 v104, v104
	v_exp_f32_e32 v106, v106
	v_exp_f32_e32 v108, v108
	v_exp_f32_e32 v110, v110
	v_exp_f32_e32 v105, v105
	v_exp_f32_e32 v107, v107
	v_exp_f32_e32 v109, v109
	v_exp_f32_e32 v111, v111
	v_pk_add_f32 v[64:65], v[64:65], v[96:97]
	v_pk_fma_f32 v[68:69], v[96:97], v[16:17], v[68:69]
	v_pk_add_f32 v[66:67], v[66:67], v[98:99]
	v_pk_add_f32 v[64:65], v[64:65], v[98:99]
	v_pk_fma_f32 v[68:69], v[98:99], v[20:21], v[68:69]
	v_pk_fma_f32 v[70:71], v[98:99], v[18:19], v[70:71]
	v_pk_add_f32 v[66:67], v[66:67], v[100:101]
	v_pk_fma_f32 v[70:71], v[100:101], v[22:23], v[70:71]
	v_sub_f32_e32 v100, v18, v17
	v_sub_f32_e32 v96, v19, v18
	v_sub_f32_e32 v102, v20, v19
	v_sub_f32_e32 v98, v21, v20
	v_sub_f32_e64 v97, v22, v21
	v_fma_f32 v100, -v100, v100, s20
	v_fma_f32 v96, -v96, v96, s20
	v_fma_f32 v102, -v102, v102, s20
	v_fma_f32 v98, -v98, v98, s20
	v_fma_f32 v97, -v97, v97, s20
	v_exp_f32_e32 v100, v100
	v_exp_f32_e32 v96, v96
	v_exp_f32_e32 v102, v102
	v_exp_f32_e32 v98, v98
	v_exp_f32_e32 v97, v97
	v_add_f32_e32 v64, v64, v104
	v_fmac_f32_e32 v68, v104, v1
	v_add_f32_e32 v66, v66, v106
	v_fmac_f32_e32 v70, v106, v3
	v_add_f32_e32 v65, v65, v108
	v_fmac_f32_e32 v69, v108, v4
	v_add_f32_e32 v67, v67, v110
	v_fmac_f32_e32 v71, v110, v6
	v_add_f32_e32 v64, v64, v105
	v_fmac_f32_e32 v68, v105, v9
	v_add_f32_e32 v66, v66, v107
	v_fmac_f32_e32 v70, v107, v11
	v_add_f32_e32 v65, v65, v109
	v_fmac_f32_e32 v69, v109, v12
	v_add_f32_e32 v67, v67, v111
	v_fmac_f32_e32 v71, v111, v14
	v_add_f32_e32 v64, v64, v100
	v_fmac_f32_e32 v68, v100, v17
	v_add_f32_e32 v65, v65, v102
	v_fmac_f32_e32 v69, v102, v20
	v_add_f32_e32 v66, v66, v102
	v_fmac_f32_e32 v70, v102, v19
	v_add_f32_e32 v67, v67, v97
	v_fmac_f32_e64 v71, v97, v22
	v_pk_add_f32 v[64:65], v[64:65], v[96:97] op_sel_hi:[1,0]
	v_pk_fma_f32 v[68:69], v[96:97], v[18:19], v[68:69] op_sel:[0,1,0] op_sel_hi:[0,0,1]
	v_pk_add_f32 v[66:67], v[66:67], v[98:99] op_sel_hi:[1,0]
	v_pk_fma_f32 v[70:71], v[98:99], v[20:21], v[70:71] op_sel:[0,1,0] op_sel_hi:[0,0,1]
	s_waitcnt vmcnt(12)
	s_nop 0
	v_mov_b32_dpp v24, v28 row_shr:1 row_mask:0xf bank_mask:0xf
	v_mov_b32_dpp v25, v29 row_shr:1 row_mask:0xf bank_mask:0xf
	v_mov_b32_dpp v30, v26 row_shl:1 row_mask:0xf bank_mask:0xf
	v_mov_b32_dpp v31, v27 row_shl:1 row_mask:0xf bank_mask:0xf
	v_pk_mul_f32 v[26:27], v[26:27], s[32:33]
	v_pk_mul_f32 v[28:29], v[28:29], s[32:33]
	v_cndmask_b32_e64 v25, v25, v24, vcc
	v_cndmask_b32_e64 v30, v30, v31, s[16:17]
	v_pk_mul_f32 v[76:77], v[26:27], s[30:31]
	v_pk_mul_f32 v[78:79], v[28:29], s[30:31]
	v_pk_mul_f32 v[24:25], v[24:25], s[32:33]
	v_pk_mul_f32 v[30:31], v[30:31], s[32:33]
	v_mov_b32_e32 v72, s30
	v_mov_b32_e32 v73, s30
	v_mov_b32_e64 v74, s30
	v_mov_b32_e32 v75, s30
	s_setprio 3
	v_pk_add_f32 v[96:97], v[26:27], v[8:9] neg_lo:[0,1] neg_hi:[0,1]
	v_pk_add_f32 v[98:99], v[26:27], v[10:11] neg_lo:[0,1] neg_hi:[0,1]
	v_pk_add_f32 v[100:101], v[28:29], v[10:11] neg_lo:[0,1] neg_hi:[0,1]
	v_pk_add_f32 v[102:103], v[26:27], v[12:13] neg_lo:[0,1] neg_hi:[0,1]
	v_pk_fma_f32 v[96:97], v[96:97], v[96:97], s[28:29] neg_lo:[1,0,0] neg_hi:[1,0,0]
	v_pk_fma_f32 v[98:99], v[98:99], v[98:99], s[22:23] neg_lo:[1,0,0] neg_hi:[1,0,0]
	v_pk_fma_f32 v[100:101], v[100:101], v[100:101], s[28:29] neg_lo:[1,0,0] neg_hi:[1,0,0]
	v_pk_fma_f32 v[102:103], v[102:103], v[102:103], s[28:29] neg_lo:[1,0,0] neg_hi:[1,0,0]
	v_exp_f32_e32 v96, v96
	v_exp_f32_e32 v97, v97
	v_exp_f32_e32 v98, v98
	v_exp_f32_e32 v99, v99
	v_exp_f32_e32 v100, v100
	v_exp_f32_e32 v101, v101
	v_exp_f32_e32 v102, v102
	v_exp_f32_e32 v103, v103
	v_pk_add_f32 v[104:105], v[28:29], v[12:13] neg_lo:[0,1] neg_hi:[0,1]
	v_pk_add_f32 v[106:107], v[28:29], v[14:15] neg_lo:[0,1] neg_hi:[0,1]
	v_pk_add_f32 v[108:109], v[26:27], v[10:11] op_sel:[1,0] op_sel_hi:[0,1] neg_lo:[0,1] neg_hi:[0,1]
	v_pk_add_f32 v[110:111], v[28:29], v[12:13] op_sel:[1,0] op_sel_hi:[0,1] neg_lo:[0,1] neg_hi:[0,1]
	v_pk_fma_f32 v[104:105], v[104:105], v[104:105], s[22:23] neg_lo:[1,0,0] neg_hi:[1,0,0]
	v_pk_fma_f32 v[106:107], v[106:107], v[106:107], s[28:29] neg_lo:[1,0,0] neg_hi:[1,0,0]
	v_pk_fma_f32 v[108:109], v[108:109], v[108:109], s[26:27] neg_lo:[1,0,0] neg_hi:[1,0,0]
	v_pk_fma_f32 v[110:111], v[110:111], v[110:111], s[26:27] neg_lo:[1,0,0] neg_hi:[1,0,0]
	v_exp_f32_e32 v104, v104
	v_exp_f32_e32 v105, v105
	v_exp_f32_e32 v106, v106
	v_exp_f32_e32 v107, v107
	v_exp_f32_e32 v108, v108
	v_exp_f32_e32 v109, v109
	v_exp_f32_e32 v110, v110
	v_exp_f32_e32 v111, v111
	v_pk_add_f32 v[72:73], v[72:73], v[96:97]
	v_pk_fma_f32 v[76:77], v[96:97], v[8:9], v[76:77]
	v_pk_add_f32 v[74:75], v[74:75], v[100:101]
	v_pk_add_f32 v[72:73], v[72:73], v[98:99]
	v_pk_fma_f32 v[76:77], v[98:99], v[10:11], v[76:77]
	v_pk_fma_f32 v[78:79], v[100:101], v[10:11], v[78:79]
	v_pk_add_f32 v[72:73], v[72:73], v[102:103]
	v_pk_fma_f32 v[76:77], v[102:103], v[12:13], v[76:77]
	v_pk_add_f32 v[96:97], v[26:27], v[16:17] neg_lo:[0,1] neg_hi:[0,1]
	v_pk_add_f32 v[98:99], v[24:25], v[18:19] neg_lo:[0,1] neg_hi:[0,1]
	v_pk_add_f32 v[100:101], v[26:27], v[18:19] neg_lo:[0,1] neg_hi:[0,1]
	v_pk_add_f32 v[102:103], v[28:29], v[18:19] neg_lo:[0,1] neg_hi:[0,1]
	v_pk_fma_f32 v[96:97], v[96:97], v[96:97], s[26:27] neg_lo:[1,0,0] neg_hi:[1,0,0]
	v_pk_fma_f32 v[98:99], v[98:99], v[98:99], s[26:27] neg_lo:[1,0,0] neg_hi:[1,0,0]
	v_pk_fma_f32 v[100:101], v[100:101], v[100:101], s[20:21] neg_lo:[1,0,0] neg_hi:[1,0,0]
	v_pk_fma_f32 v[102:103], v[102:103], v[102:103], s[26:27] neg_lo:[1,0,0] neg_hi:[1,0,0]
	v_exp_f32_e32 v96, v96
	v_exp_f32_e32 v97, v97
	v_exp_f32_e32 v98, v98
	v_exp_f32_e32 v99, v99
	v_exp_f32_e32 v100, v100
	v_exp_f32_e32 v101, v101
	v_exp_f32_e32 v102, v102
	v_exp_f32_e32 v103, v103
	v_pk_add_f32 v[74:75], v[74:75], v[104:105]
	v_pk_fma_f32 v[78:79], v[104:105], v[12:13], v[78:79]
	v_pk_add_f32 v[72:73], v[72:73], v[108:109] op_sel:[0,1] op_sel_hi:[1,0]
	v_pk_add_f32 v[74:75], v[74:75], v[106:107]
	v_pk_fma_f32 v[78:79], v[106:107], v[14:15], v[78:79]
	v_pk_fma_f32 v[76:77], v[108:109], v[10:11], v[76:77] op_sel:[1,1,0] op_sel_hi:[0,0,1]
	v_pk_add_f32 v[74:75], v[74:75], v[110:111] op_sel:[0,1] op_sel_hi:[1,0]
	v_pk_fma_f32 v[78:79], v[110:111], v[12:13], v[78:79] op_sel:[1,1,0] op_sel_hi:[0,0,1]
	v_pk_add_f32 v[104:105], v[26:27], v[20:21] neg_lo:[0,1] neg_hi:[0,1]
	v_pk_add_f32 v[106:107], v[28:29], v[20:21] neg_lo:[0,1] neg_hi:[0,1]
	v_pk_add_f32 v[108:109], v[30:31], v[20:21] neg_lo:[0,1] neg_hi:[0,1]
	v_pk_add_f32 v[110:111], v[28:29], v[22:23] neg_lo:[0,1] neg_hi:[0,1]
	v_pk_fma_f32 v[104:105], v[104:105], v[104:105], s[26:27] neg_lo:[1,0,0] neg_hi:[1,0,0]
	v_pk_fma_f32 v[106:107], v[106:107], v[106:107], s[20:21] neg_lo:[1,0,0] neg_hi:[1,0,0]
	v_pk_fma_f32 v[108:109], v[108:109], v[108:109], s[26:27] neg_lo:[1,0,0] neg_hi:[1,0,0]
	v_pk_fma_f32 v[110:111], v[110:111], v[110:111], s[26:27] neg_lo:[1,0,0] neg_hi:[1,0,0]
	v_exp_f32_e32 v104, v104
	v_exp_f32_e32 v105, v105
	v_exp_f32_e32 v106, v106
	v_exp_f32_e32 v107, v107
	v_exp_f32_e32 v108, v108
	v_exp_f32_e32 v109, v109
	v_exp_f32_e32 v110, v110
	v_exp_f32_e32 v111, v111
	v_pk_add_f32 v[72:73], v[72:73], v[96:97]
	v_pk_fma_f32 v[76:77], v[96:97], v[16:17], v[76:77]
	v_pk_add_f32 v[64:65], v[64:65], v[98:99]
	v_pk_fma_f32 v[68:69], v[98:99], v[24:25], v[68:69]
	v_pk_add_f32 v[72:73], v[72:73], v[100:101]
	v_pk_add_f32 v[64:65], v[64:65], v[100:101]
	v_pk_fma_f32 v[68:69], v[100:101], v[26:27], v[68:69]
	v_pk_fma_f32 v[76:77], v[100:101], v[18:19], v[76:77]
	v_pk_add_f32 v[64:65], v[64:65], v[102:103]
	v_pk_fma_f32 v[68:69], v[102:103], v[28:29], v[68:69]
	v_pk_add_f32 v[74:75], v[74:75], v[102:103]
	v_pk_fma_f32 v[78:79], v[102:103], v[18:19], v[78:79]
	v_pk_add_f32 v[96:97], v[26:27], v[18:19] op_sel:[1,0] op_sel_hi:[0,1] neg_lo:[0,1] neg_hi:[0,1]
	v_pk_add_f32 v[98:99], v[28:29], v[20:21] op_sel:[1,0] op_sel_hi:[0,1] neg_lo:[0,1] neg_hi:[0,1]
	v_pk_add_f32 v[100:101], v[26:27], v[24:25] neg_lo:[0,1] neg_hi:[0,1]
	v_pk_add_f32 v[102:103], v[28:29], v[26:27] neg_lo:[0,1] neg_hi:[0,1]
	v_pk_fma_f32 v[96:97], v[96:97], v[96:97], s[24:25] neg_lo:[1,0,0] neg_hi:[1,0,0]
	v_pk_fma_f32 v[98:99], v[98:99], v[98:99], s[24:25] neg_lo:[1,0,0] neg_hi:[1,0,0]
	v_pk_fma_f32 v[100:101], v[100:101], v[100:101], s[22:23] neg_lo:[1,0,0] neg_hi:[1,0,0]
	v_pk_fma_f32 v[102:103], v[102:103], v[102:103], s[22:23] neg_lo:[1,0,0] neg_hi:[1,0,0]
	v_exp_f32_e32 v96, v96
	v_exp_f32_e32 v97, v97
	v_exp_f32_e32 v98, v98
	v_exp_f32_e32 v99, v99
	v_exp_f32_e32 v100, v100
	v_exp_f32_e32 v101, v101
	v_exp_f32_e32 v102, v102
	v_exp_f32_e32 v103, v103
	v_pk_add_f32 v[66:67], v[66:67], v[104:105]
	v_pk_fma_f32 v[70:71], v[104:105], v[26:27], v[70:71]
	v_pk_add_f32 v[72:73], v[72:73], v[104:105]
	v_pk_fma_f32 v[76:77], v[104:105], v[20:21], v[76:77]
	v_pk_add_f32 v[66:67], v[66:67], v[106:107]
	v_pk_fma_f32 v[70:71], v[106:107], v[28:29], v[70:71]
	v_pk_add_f32 v[74:75], v[74:75], v[106:107]
	v_pk_fma_f32 v[78:79], v[106:107], v[20:21], v[78:79]
	v_pk_add_f32 v[66:67], v[66:67], v[108:109]
	v_pk_fma_f32 v[70:71], v[108:109], v[30:31], v[70:71]
	v_pk_add_f32 v[74:75], v[74:75], v[110:111]
	v_pk_fma_f32 v[78:79], v[110:111], v[22:23], v[78:79]
	v_pk_add_f32 v[104:105], v[30:31], v[28:29] neg_lo:[0,1] neg_hi:[0,1]
	v_pk_fma_f32 v[104:105], v[104:105], v[104:105], s[22:23] neg_lo:[1,0,0] neg_hi:[1,0,0]
	s_nop 0
	v_exp_f32_e32 v104, v104
	v_exp_f32_e64 v105, v105
	v_pk_add_f32 v[64:65], v[64:65], v[96:97]
	v_pk_fma_f32 v[68:69], v[96:97], v[26:27], v[68:69] op_sel:[0,1,0] op_sel_hi:[1,0,1]
	v_pk_add_f32 v[72:73], v[72:73], v[96:97] op_sel:[0,1] op_sel_hi:[1,0]
	v_pk_fma_f32 v[76:77], v[96:97], v[18:19], v[76:77] op_sel:[1,1,0] op_sel_hi:[0,0,1]
	v_pk_add_f32 v[66:67], v[66:67], v[98:99]
	v_pk_fma_f32 v[70:71], v[98:99], v[28:29], v[70:71] op_sel:[0,1,0] op_sel_hi:[1,0,1]
	v_pk_add_f32 v[74:75], v[74:75], v[98:99] op_sel:[0,1] op_sel_hi:[1,0]
	v_pk_fma_f32 v[78:79], v[98:99], v[20:21], v[78:79] op_sel:[1,1,0] op_sel_hi:[0,0,1]
	v_pk_add_f32 v[72:73], v[72:73], v[100:101]
	v_pk_fma_f32 v[76:77], v[100:101], v[24:25], v[76:77]
	v_pk_add_f32 v[74:75], v[74:75], v[102:103]
	v_pk_add_f32 v[72:73], v[72:73], v[102:103]
	v_pk_fma_f32 v[76:77], v[102:103], v[28:29], v[76:77]
	v_pk_fma_f32 v[78:79], v[102:103], v[26:27], v[78:79]
	s_nop 0
	v_sub_f32_e32 v96, v26, v9
	v_sub_f32_e32 v98, v28, v11
	v_sub_f32_e32 v100, v27, v12
	v_sub_f32_e32 v102, v29, v14
	v_sub_f32_e32 v97, v26, v17
	v_sub_f32_e32 v99, v25, v18
	v_sub_f32_e32 v101, v28, v19
	v_sub_f32_e64 v103, v27, v20
	v_fma_f32 v96, -v96, v96, s26
	v_fma_f32 v98, -v98, v98, s26
	v_fma_f32 v100, -v100, v100, s26
	v_fma_f32 v102, -v102, v102, s26
	v_fma_f32 v97, -v97, v97, s24
	v_fma_f32 v99, -v99, v99, s24
	v_fma_f32 v101, -v101, v101, s24
	v_fma_f32 v103, -v103, v103, s24
	v_exp_f32_e32 v96, v96
	v_exp_f32_e32 v98, v98
	v_exp_f32_e32 v100, v100
	v_exp_f32_e32 v102, v102
	v_exp_f32_e32 v97, v97
	v_exp_f32_e32 v99, v99
	v_exp_f32_e32 v101, v101
	v_exp_f32_e32 v103, v103
	v_pk_add_f32 v[74:75], v[74:75], v[104:105]
	v_pk_fma_f32 v[78:79], v[104:105], v[30:31], v[78:79]
	v_sub_f32_e32 v108, v30, v21
	v_sub_f32_e32 v110, v29, v22
	v_sub_f32_e32 v105, v26, v25
	v_sub_f32_e32 v104, v27, v26
	v_sub_f32_e32 v107, v28, v27
	v_sub_f32_e32 v106, v29, v28
	v_sub_f32_e64 v109, v30, v29
	v_fma_f32 v108, -v108, v108, s24
	v_fma_f32 v110, -v110, v110, s24
	v_fma_f32 v105, -v105, v105, s20
	v_fma_f32 v104, -v104, v104, s20
	v_fma_f32 v107, -v107, v107, s20
	v_fma_f32 v106, -v106, v106, s20
	v_fma_f32 v109, -v109, v109, s20
	v_exp_f32_e32 v108, v108
	v_exp_f32_e32 v110, v110
	v_exp_f32_e32 v105, v105
	v_exp_f32_e32 v104, v104
	v_exp_f32_e32 v107, v107
	v_exp_f32_e32 v106, v106
	v_exp_f32_e32 v109, v109
	v_add_f32_e32 v72, v72, v96
	v_fmac_f32_e32 v76, v96, v9
	v_add_f32_e32 v74, v74, v98
	v_fmac_f32_e32 v78, v98, v11
	v_add_f32_e32 v73, v73, v100
	v_fmac_f32_e32 v77, v100, v12
	v_add_f32_e32 v75, v75, v102
	v_fmac_f32_e32 v79, v102, v14
	v_add_f32_e32 v72, v72, v97
	v_fmac_f32_e32 v76, v97, v17
	v_add_f32_e32 v64, v64, v99
	v_fmac_f32_e32 v68, v99, v25
	v_add_f32_e32 v65, v65, v101
	v_fmac_f32_e32 v69, v101, v28
	v_add_f32_e32 v74, v74, v101
	v_fmac_f32_e32 v78, v101, v19
	v_add_f32_e32 v66, v66, v103
	v_fmac_f32_e32 v70, v103, v27
	v_add_f32_e32 v73, v73, v103
	v_fmac_f32_e32 v77, v103, v20
	v_add_f32_e32 v67, v67, v108
	v_fmac_f32_e32 v71, v108, v30
	v_add_f32_e32 v75, v75, v110
	v_fmac_f32_e32 v79, v110, v22
	v_add_f32_e32 v72, v72, v105
	v_fmac_f32_e32 v76, v105, v25
	v_add_f32_e32 v73, v73, v107
	v_fmac_f32_e32 v77, v107, v28
	v_add_f32_e32 v74, v74, v107
	v_fmac_f32_e32 v78, v107, v27
	v_add_f32_e32 v75, v75, v109
	v_fmac_f32_e64 v79, v109, v30
	v_pk_add_f32 v[72:73], v[72:73], v[104:105] op_sel_hi:[1,0]
	v_pk_fma_f32 v[76:77], v[104:105], v[26:27], v[76:77] op_sel:[0,1,0] op_sel_hi:[0,0,1]
	v_pk_add_f32 v[74:75], v[74:75], v[106:107] op_sel_hi:[1,0]
	v_pk_fma_f32 v[78:79], v[106:107], v[28:29], v[78:79] op_sel:[0,1,0] op_sel_hi:[0,0,1]
	s_waitcnt vmcnt(9)
	s_nop 0
	v_mov_b32_dpp v32, v36 row_shr:1 row_mask:0xf bank_mask:0xf
	v_mov_b32_dpp v33, v37 row_shr:1 row_mask:0xf bank_mask:0xf
	v_mov_b32_dpp v38, v34 row_shl:1 row_mask:0xf bank_mask:0xf
	v_mov_b32_dpp v39, v35 row_shl:1 row_mask:0xf bank_mask:0xf
	v_pk_mul_f32 v[34:35], v[34:35], s[32:33]
	v_pk_mul_f32 v[36:37], v[36:37], s[32:33]
	v_cndmask_b32_e64 v33, v33, v32, vcc
	v_cndmask_b32_e64 v38, v38, v39, s[16:17]
	v_pk_mul_f32 v[84:85], v[34:35], s[30:31]
	v_pk_mul_f32 v[86:87], v[36:37], s[30:31]
	v_pk_mul_f32 v[32:33], v[32:33], s[32:33]
	v_pk_mul_f32 v[38:39], v[38:39], s[32:33]
	v_mov_b32_e32 v80, s30
	v_mov_b32_e32 v81, s30
	v_mov_b32_e64 v82, s30
	v_mov_b32_e32 v83, s30
	s_setprio 2
	v_pk_add_f32 v[96:97], v[34:35], v[16:17] neg_lo:[0,1] neg_hi:[0,1]
	v_pk_add_f32 v[98:99], v[32:33], v[18:19] neg_lo:[0,1] neg_hi:[0,1]
	v_pk_add_f32 v[100:101], v[34:35], v[18:19] neg_lo:[0,1] neg_hi:[0,1]
	v_pk_add_f32 v[102:103], v[36:37], v[18:19] neg_lo:[0,1] neg_hi:[0,1]
	v_pk_fma_f32 v[96:97], v[96:97], v[96:97], s[28:29] neg_lo:[1,0,0] neg_hi:[1,0,0]
	v_pk_fma_f32 v[98:99], v[98:99], v[98:99], s[28:29] neg_lo:[1,0,0] neg_hi:[1,0,0]
	v_pk_fma_f32 v[100:101], v[100:101], v[100:101], s[22:23] neg_lo:[1,0,0] neg_hi:[1,0,0]
	v_pk_fma_f32 v[102:103], v[102:103], v[102:103], s[28:29] neg_lo:[1,0,0] neg_hi:[1,0,0]
	v_exp_f32_e32 v96, v96
	v_exp_f32_e32 v97, v97
	v_exp_f32_e32 v98, v98
	v_exp_f32_e32 v99, v99
	v_exp_f32_e32 v100, v100
	v_exp_f32_e32 v101, v101
	v_exp_f32_e32 v102, v102
	v_exp_f32_e32 v103, v103
	v_pk_add_f32 v[104:105], v[34:35], v[20:21] neg_lo:[0,1] neg_hi:[0,1]
	v_pk_add_f32 v[106:107], v[36:37], v[20:21] neg_lo:[0,1] neg_hi:[0,1]
	v_pk_add_f32 v[108:109], v[38:39], v[20:21] neg_lo:[0,1] neg_hi:[0,1]
	v_pk_add_f32 v[110:111], v[36:37], v[22:23] neg_lo:[0,1] neg_hi:[0,1]
	v_pk_fma_f32 v[104:105], v[104:105], v[104:105], s[28:29] neg_lo:[1,0,0] neg_hi:[1,0,0]
	v_pk_fma_f32 v[106:107], v[106:107], v[106:107], s[22:23] neg_lo:[1,0,0] neg_hi:[1,0,0]
	v_pk_fma_f32 v[108:109], v[108:109], v[108:109], s[28:29] neg_lo:[1,0,0] neg_hi:[1,0,0]
	v_pk_fma_f32 v[110:111], v[110:111], v[110:111], s[28:29] neg_lo:[1,0,0] neg_hi:[1,0,0]
	v_exp_f32_e32 v104, v104
	v_exp_f32_e32 v105, v105
	v_exp_f32_e32 v106, v106
	v_exp_f32_e32 v107, v107
	v_exp_f32_e32 v108, v108
	v_exp_f32_e32 v109, v109
	v_exp_f32_e32 v110, v110
	v_exp_f32_e32 v111, v111
	v_pk_add_f32 v[80:81], v[80:81], v[96:97]
	v_pk_fma_f32 v[84:85], v[96:97], v[16:17], v[84:85]
	v_pk_add_f32 v[64:65], v[64:65], v[98:99]
	v_pk_fma_f32 v[68:69], v[98:99], v[32:33], v[68:69]
	v_pk_add_f32 v[80:81], v[80:81], v[100:101]
	v_pk_add_f32 v[64:65], v[64:65], v[100:101]
	v_pk_fma_f32 v[68:69], v[100:101], v[34:35], v[68:69]
	v_pk_fma_f32 v[84:85], v[100:101], v[18:19], v[84:85]
	v_pk_add_f32 v[64:65], v[64:65], v[102:103]
	v_pk_fma_f32 v[68:69], v[102:103], v[36:37], v[68:69]
	v_pk_add_f32 v[82:83], v[82:83], v[102:103]
	v_pk_fma_f32 v[86:87], v[102:103], v[18:19], v[86:87]
	v_pk_add_f32 v[96:97], v[34:35], v[18:19] op_sel:[1,0] op_sel_hi:[0,1] neg_lo:[0,1] neg_hi:[0,1]
	v_pk_add_f32 v[98:99], v[36:37], v[20:21] op_sel:[1,0] op_sel_hi:[0,1] neg_lo:[0,1] neg_hi:[0,1]
	v_pk_add_f32 v[100:101], v[34:35], v[24:25] neg_lo:[0,1] neg_hi:[0,1]
	v_pk_add_f32 v[102:103], v[32:33], v[26:27] neg_lo:[0,1] neg_hi:[0,1]
	v_pk_fma_f32 v[96:97], v[96:97], v[96:97], s[26:27] neg_lo:[1,0,0] neg_hi:[1,0,0]
	v_pk_fma_f32 v[98:99], v[98:99], v[98:99], s[26:27] neg_lo:[1,0,0] neg_hi:[1,0,0]
	v_pk_fma_f32 v[100:101], v[100:101], v[100:101], s[26:27] neg_lo:[1,0,0] neg_hi:[1,0,0]
	v_pk_fma_f32 v[102:103], v[102:103], v[102:103], s[26:27] neg_lo:[1,0,0] neg_hi:[1,0,0]
	v_exp_f32_e32 v96, v96
	v_exp_f32_e32 v97, v97
	v_exp_f32_e32 v98, v98
	v_exp_f32_e32 v99, v99
	v_exp_f32_e32 v100, v100
	v_exp_f32_e32 v101, v101
	v_exp_f32_e32 v102, v102
	v_exp_f32_e32 v103, v103
	v_pk_add_f32 v[66:67], v[66:67], v[104:105]
	v_pk_fma_f32 v[70:71], v[104:105], v[34:35], v[70:71]
	v_pk_add_f32 v[80:81], v[80:81], v[104:105]
	v_pk_fma_f32 v[84:85], v[104:105], v[20:21], v[84:85]
	v_pk_add_f32 v[66:67], v[66:67], v[106:107]
	v_pk_fma_f32 v[70:71], v[106:107], v[36:37], v[70:71]
	v_pk_add_f32 v[82:83], v[82:83], v[106:107]
	v_pk_fma_f32 v[86:87], v[106:107], v[20:21], v[86:87]
	v_pk_add_f32 v[66:67], v[66:67], v[108:109]
	v_pk_fma_f32 v[70:71], v[108:109], v[38:39], v[70:71]
	v_pk_add_f32 v[82:83], v[82:83], v[110:111]
	v_pk_fma_f32 v[86:87], v[110:111], v[22:23], v[86:87]
	v_pk_add_f32 v[104:105], v[34:35], v[26:27] neg_lo:[0,1] neg_hi:[0,1]
	v_pk_add_f32 v[106:107], v[36:37], v[26:27] neg_lo:[0,1] neg_hi:[0,1]
	v_pk_add_f32 v[108:109], v[34:35], v[28:29] neg_lo:[0,1] neg_hi:[0,1]
	v_pk_add_f32 v[110:111], v[36:37], v[28:29] neg_lo:[0,1] neg_hi:[0,1]
	v_pk_fma_f32 v[104:105], v[104:105], v[104:105], s[20:21] neg_lo:[1,0,0] neg_hi:[1,0,0]
	v_pk_fma_f32 v[106:107], v[106:107], v[106:107], s[26:27] neg_lo:[1,0,0] neg_hi:[1,0,0]
	v_pk_fma_f32 v[108:109], v[108:109], v[108:109], s[26:27] neg_lo:[1,0,0] neg_hi:[1,0,0]
	v_pk_fma_f32 v[110:111], v[110:111], v[110:111], s[20:21] neg_lo:[1,0,0] neg_hi:[1,0,0]
	v_exp_f32_e32 v104, v104
	v_exp_f32_e32 v105, v105
	v_exp_f32_e32 v106, v106
	v_exp_f32_e32 v107, v107
	v_exp_f32_e32 v108, v108
	v_exp_f32_e32 v109, v109
	v_exp_f32_e32 v110, v110
	v_exp_f32_e32 v111, v111
	v_pk_add_f32 v[64:65], v[64:65], v[96:97]
	v_pk_fma_f32 v[68:69], v[96:97], v[34:35], v[68:69] op_sel:[0,1,0] op_sel_hi:[1,0,1]
	v_pk_add_f32 v[80:81], v[80:81], v[96:97] op_sel:[0,1] op_sel_hi:[1,0]
	v_pk_fma_f32 v[84:85], v[96:97], v[18:19], v[84:85] op_sel:[1,1,0] op_sel_hi:[0,0,1]
	v_pk_add_f32 v[66:67], v[66:67], v[98:99]
	v_pk_fma_f32 v[70:71], v[98:99], v[36:37], v[70:71] op_sel:[0,1,0] op_sel_hi:[1,0,1]
	v_pk_add_f32 v[82:83], v[82:83], v[98:99] op_sel:[0,1] op_sel_hi:[1,0]
	v_pk_fma_f32 v[86:87], v[98:99], v[20:21], v[86:87] op_sel:[1,1,0] op_sel_hi:[0,0,1]
	v_pk_add_f32 v[80:81], v[80:81], v[100:101]
	v_pk_fma_f32 v[84:85], v[100:101], v[24:25], v[84:85]
	v_pk_add_f32 v[72:73], v[72:73], v[102:103]
	v_pk_fma_f32 v[76:77], v[102:103], v[32:33], v[76:77]
	v_pk_add_f32 v[96:97], v[38:39], v[28:29] neg_lo:[0,1] neg_hi:[0,1]
	v_pk_add_f32 v[98:99], v[36:37], v[30:31] neg_lo:[0,1] neg_hi:[0,1]
	v_pk_add_f32 v[100:101], v[34:35], v[26:27] op_sel:[1,0] op_sel_hi:[0,1] neg_lo:[0,1] neg_hi:[0,1]
	v_pk_add_f32 v[102:103], v[36:37], v[28:29] op_sel:[1,0] op_sel_hi:[0,1] neg_lo:[0,1] neg_hi:[0,1]
	v_pk_fma_f32 v[96:97], v[96:97], v[96:97], s[26:27] neg_lo:[1,0,0] neg_hi:[1,0,0]
	v_pk_fma_f32 v[98:99], v[98:99], v[98:99], s[26:27] neg_lo:[1,0,0] neg_hi:[1,0,0]
	v_pk_fma_f32 v[100:101], v[100:101], v[100:101], s[24:25] neg_lo:[1,0,0] neg_hi:[1,0,0]
	v_pk_fma_f32 v[102:103], v[102:103], v[102:103], s[24:25] neg_lo:[1,0,0] neg_hi:[1,0,0]
	v_exp_f32_e32 v96, v96
	v_exp_f32_e32 v97, v97
	v_exp_f32_e32 v98, v98
	v_exp_f32_e32 v99, v99
	v_exp_f32_e32 v100, v100
	v_exp_f32_e32 v101, v101
	v_exp_f32_e32 v102, v102
	v_exp_f32_e32 v103, v103
	v_pk_add_f32 v[72:73], v[72:73], v[104:105]
	v_pk_fma_f32 v[76:77], v[104:105], v[34:35], v[76:77]
	v_pk_add_f32 v[80:81], v[80:81], v[104:105]
	v_pk_fma_f32 v[84:85], v[104:105], v[26:27], v[84:85]
	v_pk_add_f32 v[72:73], v[72:73], v[106:107]
	v_pk_fma_f32 v[76:77], v[106:107], v[36:37], v[76:77]
	v_pk_add_f32 v[82:83], v[82:83], v[106:107]
	v_pk_fma_f32 v[86:87], v[106:107], v[26:27], v[86:87]
	v_pk_add_f32 v[74:75], v[74:75], v[108:109]
	v_pk_fma_f32 v[78:79], v[108:109], v[34:35], v[78:79]
	v_pk_add_f32 v[80:81], v[80:81], v[108:109]
	v_pk_fma_f32 v[84:85], v[108:109], v[28:29], v[84:85]
	v_pk_add_f32 v[74:75], v[74:75], v[110:111]
	v_pk_fma_f32 v[78:79], v[110:111], v[36:37], v[78:79]
	v_pk_add_f32 v[82:83], v[82:83], v[110:111]
	v_pk_fma_f32 v[86:87], v[110:111], v[28:29], v[86:87]
	v_pk_add_f32 v[104:105], v[34:35], v[32:33] neg_lo:[0,1] neg_hi:[0,1]
	v_pk_add_f32 v[106:107], v[36:37], v[34:35] neg_lo:[0,1] neg_hi:[0,1]
	v_pk_add_f32 v[108:109], v[38:39], v[36:37] neg_lo:[0,1] neg_hi:[0,1]
	v_pk_fma_f32 v[104:105], v[104:105], v[104:105], s[22:23] neg_lo:[1,0,0] neg_hi:[1,0,0]
	v_pk_fma_f32 v[106:107], v[106:107], v[106:107], s[22:23] neg_lo:[1,0,0] neg_hi:[1,0,0]
	v_pk_fma_f32 v[108:109], v[108:109], v[108:109], s[22:23] neg_lo:[1,0,0] neg_hi:[1,0,0]
	v_exp_f32_e32 v104, v104
	v_exp_f32_e32 v105, v105
	v_exp_f32_e32 v106, v106
	v_exp_f32_e32 v107, v107
	v_exp_f32_e32 v108, v108
	v_exp_f32_e32 v109, v109
	v_pk_add_f32 v[74:75], v[74:75], v[96:97]
	v_pk_fma_f32 v[78:79], v[96:97], v[38:39], v[78:79]
	v_pk_add_f32 v[82:83], v[82:83], v[98:99]
	v_pk_fma_f32 v[86:87], v[98:99], v[30:31], v[86:87]
	v_pk_add_f32 v[72:73], v[72:73], v[100:101]
	v_pk_fma_f32 v[76:77], v[100:101], v[34:35], v[76:77] op_sel:[0,1,0] op_sel_hi:[1,0,1]
	v_pk_add_f32 v[80:81], v[80:81], v[100:101] op_sel:[0,1] op_sel_hi:[1,0]
	v_pk_fma_f32 v[84:85], v[100:101], v[26:27], v[84:85] op_sel:[1,1,0] op_sel_hi:[0,0,1]
	v_pk_add_f32 v[74:75], v[74:75], v[102:103]
	v_pk_fma_f32 v[78:79], v[102:103], v[36:37], v[78:79] op_sel:[0,1,0] op_sel_hi:[1,0,1]
	v_pk_add_f32 v[82:83], v[82:83], v[102:103] op_sel:[0,1] op_sel_hi:[1,0]
	v_pk_fma_f32 v[86:87], v[102:103], v[28:29], v[86:87] op_sel:[1,1,0] op_sel_hi:[0,0,1]
	v_sub_f32_e32 v96, v34, v17
	v_sub_f32_e32 v98, v33, v18
	v_sub_f32_e32 v100, v36, v19
	v_sub_f32_e32 v102, v35, v20
	v_sub_f32_e32 v97, v38, v21
	v_sub_f32_e32 v99, v37, v22
	v_sub_f32_e32 v101, v34, v25
	v_sub_f32_e32 v103, v33, v26
	v_fma_f32 v96, -v96, v96, s26
	v_fma_f32 v98, -v98, v98, s26
	v_fma_f32 v100, -v100, v100, s26
	v_fma_f32 v102, -v102, v102, s26
	v_fma_f32 v97, -v97, v97, s26
	v_fma_f32 v99, -v99, v99, s26
	v_fma_f32 v101, -v101, v101, s24
	v_fma_f32 v103, -v103, v103, s24
	v_exp_f32_e32 v96, v96
	v_exp_f32_e32 v98, v98
	v_exp_f32_e32 v100, v100
	v_exp_f32_e32 v102, v102
	v_exp_f32_e32 v97, v97
	v_exp_f32_e32 v99, v99
	v_exp_f32_e32 v101, v101
	v_exp_f32_e32 v103, v103
	v_pk_add_f32 v[80:81], v[80:81], v[104:105]
	v_pk_fma_f32 v[84:85], v[104:105], v[32:33], v[84:85]
	v_pk_add_f32 v[82:83], v[82:83], v[106:107]
	v_pk_add_f32 v[80:81], v[80:81], v[106:107]
	v_pk_fma_f32 v[84:85], v[106:107], v[36:37], v[84:85]
	v_pk_fma_f32 v[86:87], v[106:107], v[34:35], v[86:87]
	v_pk_add_f32 v[82:83], v[82:83], v[108:109]
	v_pk_fma_f32 v[86:87], v[108:109], v[38:39], v[86:87]
	v_sub_f32_e32 v108, v36, v27
	v_sub_f32_e32 v110, v35, v28
	v_sub_f32_e32 v105, v38, v29
	v_sub_f32_e32 v107, v37, v30
	v_sub_f32_e32 v109, v34, v33
	v_sub_f32_e32 v104, v35, v34
	v_sub_f32_e32 v111, v36, v35
	v_sub_f32_e32 v106, v37, v36
	v_fma_f32 v108, -v108, v108, s24
	v_fma_f32 v110, -v110, v110, s24
	v_fma_f32 v105, -v105, v105, s24
	v_fma_f32 v107, -v107, v107, s24
	v_fma_f32 v109, -v109, v109, s20
	v_fma_f32 v104, -v104, v104, s20
	v_fma_f32 v111, -v111, v111, s20
	v_fma_f32 v106, -v106, v106, s20
	v_exp_f32_e32 v108, v108
	v_exp_f32_e32 v110, v110
	v_exp_f32_e32 v105, v105
	v_exp_f32_e32 v107, v107
	v_exp_f32_e32 v109, v109
	v_exp_f32_e32 v104, v104
	v_exp_f32_e32 v111, v111
	v_exp_f32_e32 v106, v106
	v_add_f32_e32 v80, v80, v96
	v_fmac_f32_e32 v84, v96, v17
	v_add_f32_e32 v64, v64, v98
	v_fmac_f32_e32 v68, v98, v33
	v_add_f32_e32 v65, v65, v100
	v_fmac_f32_e32 v69, v100, v36
	v_add_f32_e32 v82, v82, v100
	v_fmac_f32_e32 v86, v100, v19
	v_add_f32_e32 v66, v66, v102
	v_fmac_f32_e32 v70, v102, v35
	v_add_f32_e32 v81, v81, v102
	v_fmac_f32_e32 v85, v102, v20
	v_add_f32_e32 v67, v67, v97
	v_fmac_f32_e32 v71, v97, v38
	v_add_f32_e32 v83, v83, v99
	v_fmac_f32_e32 v87, v99, v22
	v_add_f32_e32 v80, v80, v101
	v_fmac_f32_e32 v84, v101, v25
	v_add_f32_e32 v72, v72, v103
	v_fmac_f32_e32 v76, v103, v33
	v_sub_f32_e64 v96, v38, v37
	v_fma_f32 v96, -v96, v96, s20
	s_nop 0
	v_exp_f32_e32 v96, v96
	v_add_f32_e32 v73, v73, v108
	v_fmac_f32_e32 v77, v108, v36
	v_add_f32_e32 v82, v82, v108
	v_fmac_f32_e32 v86, v108, v27
	v_add_f32_e32 v74, v74, v110
	v_fmac_f32_e32 v78, v110, v35
	v_add_f32_e32 v81, v81, v110
	v_fmac_f32_e32 v85, v110, v28
	v_add_f32_e32 v75, v75, v105
	v_fmac_f32_e32 v79, v105, v38
	v_add_f32_e32 v83, v83, v107
	v_fmac_f32_e32 v87, v107, v30
	v_add_f32_e32 v80, v80, v109
	v_fmac_f32_e32 v84, v109, v33
	v_add_f32_e32 v81, v81, v111
	v_fmac_f32_e32 v85, v111, v36
	v_add_f32_e32 v82, v82, v111
	v_fmac_f32_e32 v86, v111, v35
	v_pk_add_f32 v[80:81], v[80:81], v[104:105] op_sel_hi:[1,0]
	v_pk_fma_f32 v[84:85], v[104:105], v[34:35], v[84:85] op_sel:[0,1,0] op_sel_hi:[0,0,1]
	v_pk_add_f32 v[82:83], v[82:83], v[106:107] op_sel_hi:[1,0]
	v_pk_fma_f32 v[86:87], v[106:107], v[36:37], v[86:87] op_sel:[0,1,0] op_sel_hi:[0,0,1]
	s_nop 0
	v_add_f32_e32 v83, v83, v96
	v_fmac_f32_e32 v87, v96, v38
	v_rcp_f32_e32 v96, v64
	v_rcp_f32_e32 v97, v65
	v_rcp_f32_e32 v98, v66
	v_rcp_f32_e64 v99, v67
	v_pk_mul_f32 v[68:69], v[68:69], s[34:35]
	v_pk_mul_f32 v[70:71], v[70:71], s[34:35]
	v_pk_mul_f32 v[68:69], v[68:69], v[96:97]
	v_pk_mul_f32 v[70:71], v[70:71], v[98:99]
	s_nop 0
	s_nop 0
	buffer_store_dwordx4 v[68:71], v114, s[12:15], 0 offen sc1
	s_waitcnt vmcnt(7)
	s_nop 0
	v_mov_b32_dpp v40, v44 row_shr:1 row_mask:0xf bank_mask:0xf
	v_mov_b32_dpp v41, v45 row_shr:1 row_mask:0xf bank_mask:0xf
	v_mov_b32_dpp v46, v42 row_shl:1 row_mask:0xf bank_mask:0xf
	v_mov_b32_dpp v47, v43 row_shl:1 row_mask:0xf bank_mask:0xf
	v_pk_mul_f32 v[42:43], v[42:43], s[32:33]
	v_pk_mul_f32 v[44:45], v[44:45], s[32:33]
	v_cndmask_b32_e64 v41, v41, v40, vcc
	v_cndmask_b32_e64 v46, v46, v47, s[16:17]
	v_pk_mul_f32 v[92:93], v[42:43], s[30:31]
	v_pk_mul_f32 v[94:95], v[44:45], s[30:31]
	v_pk_mul_f32 v[40:41], v[40:41], s[32:33]
	v_pk_mul_f32 v[46:47], v[46:47], s[32:33]
	v_mov_b32_e32 v88, s30
	v_mov_b32_e32 v89, s30
	v_mov_b32_e64 v90, s30
	v_mov_b32_e32 v91, s30
	s_setprio 1
	v_pk_add_f32 v[96:97], v[42:43], v[24:25] neg_lo:[0,1] neg_hi:[0,1]
	v_pk_add_f32 v[98:99], v[40:41], v[26:27] neg_lo:[0,1] neg_hi:[0,1]
	v_pk_add_f32 v[100:101], v[42:43], v[26:27] neg_lo:[0,1] neg_hi:[0,1]
	v_pk_add_f32 v[102:103], v[44:45], v[26:27] neg_lo:[0,1] neg_hi:[0,1]
	v_pk_fma_f32 v[96:97], v[96:97], v[96:97], s[28:29] neg_lo:[1,0,0] neg_hi:[1,0,0]
	v_pk_fma_f32 v[98:99], v[98:99], v[98:99], s[28:29] neg_lo:[1,0,0] neg_hi:[1,0,0]
	v_pk_fma_f32 v[100:101], v[100:101], v[100:101], s[22:23] neg_lo:[1,0,0] neg_hi:[1,0,0]
	v_pk_fma_f32 v[102:103], v[102:103], v[102:103], s[28:29] neg_lo:[1,0,0] neg_hi:[1,0,0]
	v_exp_f32_e32 v96, v96
	v_exp_f32_e32 v97, v97
	v_exp_f32_e32 v98, v98
	v_exp_f32_e32 v99, v99
	v_exp_f32_e32 v100, v100
	v_exp_f32_e32 v101, v101
	v_exp_f32_e32 v102, v102
	v_exp_f32_e32 v103, v103
	v_pk_add_f32 v[104:105], v[42:43], v[28:29] neg_lo:[0,1] neg_hi:[0,1]
	v_pk_add_f32 v[106:107], v[44:45], v[28:29] neg_lo:[0,1] neg_hi:[0,1]
	v_pk_add_f32 v[108:109], v[46:47], v[28:29] neg_lo:[0,1] neg_hi:[0,1]
	v_pk_add_f32 v[110:111], v[44:45], v[30:31] neg_lo:[0,1] neg_hi:[0,1]
	v_pk_fma_f32 v[104:105], v[104:105], v[104:105], s[28:29] neg_lo:[1,0,0] neg_hi:[1,0,0]
	v_pk_fma_f32 v[106:107], v[106:107], v[106:107], s[22:23] neg_lo:[1,0,0] neg_hi:[1,0,0]
	v_pk_fma_f32 v[108:109], v[108:109], v[108:109], s[28:29] neg_lo:[1,0,0] neg_hi:[1,0,0]
	v_pk_fma_f32 v[110:111], v[110:111], v[110:111], s[28:29] neg_lo:[1,0,0] neg_hi:[1,0,0]
	v_exp_f32_e32 v104, v104
	v_exp_f32_e32 v105, v105
	v_exp_f32_e32 v106, v106
	v_exp_f32_e32 v107, v107
	v_exp_f32_e32 v108, v108
	v_exp_f32_e32 v109, v109
	v_exp_f32_e32 v110, v110
	v_exp_f32_e32 v111, v111
	v_pk_add_f32 v[88:89], v[88:89], v[96:97]
	v_pk_fma_f32 v[92:93], v[96:97], v[24:25], v[92:93]
	v_pk_add_f32 v[72:73], v[72:73], v[98:99]
	v_pk_fma_f32 v[76:77], v[98:99], v[40:41], v[76:77]
	v_pk_add_f32 v[88:89], v[88:89], v[100:101]
	v_pk_add_f32 v[72:73], v[72:73], v[100:101]
	v_pk_fma_f32 v[76:77], v[100:101], v[42:43], v[76:77]
	v_pk_fma_f32 v[92:93], v[100:101], v[26:27], v[92:93]
	v_pk_add_f32 v[72:73], v[72:73], v[102:103]
	v_pk_fma_f32 v[76:77], v[102:103], v[44:45], v[76:77]
	v_pk_add_f32 v[90:91], v[90:91], v[102:103]
	v_pk_fma_f32 v[94:95], v[102:103], v[26:27], v[94:95]
	v_pk_add_f32 v[96:97], v[42:43], v[26:27] op_sel:[1,0] op_sel_hi:[0,1] neg_lo:[0,1] neg_hi:[0,1]
	v_pk_add_f32 v[98:99], v[44:45], v[28:29] op_sel:[1,0] op_sel_hi:[0,1] neg_lo:[0,1] neg_hi:[0,1]
	v_pk_add_f32 v[100:101], v[42:43], v[32:33] neg_lo:[0,1] neg_hi:[0,1]
	v_pk_add_f32 v[102:103], v[40:41], v[34:35] neg_lo:[0,1] neg_hi:[0,1]
	v_pk_fma_f32 v[96:97], v[96:97], v[96:97], s[26:27] neg_lo:[1,0,0] neg_hi:[1,0,0]
	v_pk_fma_f32 v[98:99], v[98:99], v[98:99], s[26:27] neg_lo:[1,0,0] neg_hi:[1,0,0]
	v_pk_fma_f32 v[100:101], v[100:101], v[100:101], s[26:27] neg_lo:[1,0,0] neg_hi:[1,0,0]
	v_pk_fma_f32 v[102:103], v[102:103], v[102:103], s[26:27] neg_lo:[1,0,0] neg_hi:[1,0,0]
	v_exp_f32_e32 v96, v96
	v_exp_f32_e32 v97, v97
	v_exp_f32_e32 v98, v98
	v_exp_f32_e32 v99, v99
	v_exp_f32_e32 v100, v100
	v_exp_f32_e32 v101, v101
	v_exp_f32_e32 v102, v102
	v_exp_f32_e32 v103, v103
	v_pk_add_f32 v[74:75], v[74:75], v[104:105]
	v_pk_fma_f32 v[78:79], v[104:105], v[42:43], v[78:79]
	v_pk_add_f32 v[88:89], v[88:89], v[104:105]
	v_pk_fma_f32 v[92:93], v[104:105], v[28:29], v[92:93]
	v_pk_add_f32 v[74:75], v[74:75], v[106:107]
	v_pk_fma_f32 v[78:79], v[106:107], v[44:45], v[78:79]
	v_pk_add_f32 v[90:91], v[90:91], v[106:107]
	v_pk_fma_f32 v[94:95], v[106:107], v[28:29], v[94:95]
	v_pk_add_f32 v[74:75], v[74:75], v[108:109]
	v_pk_fma_f32 v[78:79], v[108:109], v[46:47], v[78:79]
	v_pk_add_f32 v[90:91], v[90:91], v[110:111]
	v_pk_fma_f32 v[94:95], v[110:111], v[30:31], v[94:95]
	v_pk_add_f32 v[104:105], v[42:43], v[34:35] neg_lo:[0,1] neg_hi:[0,1]
	v_pk_add_f32 v[106:107], v[44:45], v[34:35] neg_lo:[0,1] neg_hi:[0,1]
	v_pk_add_f32 v[108:109], v[42:43], v[36:37] neg_lo:[0,1] neg_hi:[0,1]
	v_pk_add_f32 v[110:111], v[44:45], v[36:37] neg_lo:[0,1] neg_hi:[0,1]
	v_pk_fma_f32 v[104:105], v[104:105], v[104:105], s[20:21] neg_lo:[1,0,0] neg_hi:[1,0,0]
	v_pk_fma_f32 v[106:107], v[106:107], v[106:107], s[26:27] neg_lo:[1,0,0] neg_hi:[1,0,0]
	v_pk_fma_f32 v[108:109], v[108:109], v[108:109], s[26:27] neg_lo:[1,0,0] neg_hi:[1,0,0]
	v_pk_fma_f32 v[110:111], v[110:111], v[110:111], s[20:21] neg_lo:[1,0,0] neg_hi:[1,0,0]
	v_exp_f32_e32 v104, v104
	v_exp_f32_e32 v105, v105
	v_exp_f32_e32 v106, v106
	v_exp_f32_e32 v107, v107
	v_exp_f32_e32 v108, v108
	v_exp_f32_e32 v109, v109
	v_exp_f32_e32 v110, v110
	v_exp_f32_e32 v111, v111
	v_pk_add_f32 v[72:73], v[72:73], v[96:97]
	v_pk_fma_f32 v[76:77], v[96:97], v[42:43], v[76:77] op_sel:[0,1,0] op_sel_hi:[1,0,1]
	v_pk_add_f32 v[88:89], v[88:89], v[96:97] op_sel:[0,1] op_sel_hi:[1,0]
	v_pk_fma_f32 v[92:93], v[96:97], v[26:27], v[92:93] op_sel:[1,1,0] op_sel_hi:[0,0,1]
	v_pk_add_f32 v[74:75], v[74:75], v[98:99]
	v_pk_fma_f32 v[78:79], v[98:99], v[44:45], v[78:79] op_sel:[0,1,0] op_sel_hi:[1,0,1]
	v_pk_add_f32 v[90:91], v[90:91], v[98:99] op_sel:[0,1] op_sel_hi:[1,0]
	v_pk_fma_f32 v[94:95], v[98:99], v[28:29], v[94:95] op_sel:[1,1,0] op_sel_hi:[0,0,1]
	v_pk_add_f32 v[88:89], v[88:89], v[100:101]
	v_pk_fma_f32 v[92:93], v[100:101], v[32:33], v[92:93]
	v_pk_add_f32 v[80:81], v[80:81], v[102:103]
	v_pk_fma_f32 v[84:85], v[102:103], v[40:41], v[84:85]
	v_pk_add_f32 v[96:97], v[46:47], v[36:37] neg_lo:[0,1] neg_hi:[0,1]
	v_pk_add_f32 v[98:99], v[44:45], v[38:39] neg_lo:[0,1] neg_hi:[0,1]
	v_pk_add_f32 v[100:101], v[42:43], v[34:35] op_sel:[1,0] op_sel_hi:[0,1] neg_lo:[0,1] neg_hi:[0,1]
	v_pk_add_f32 v[102:103], v[44:45], v[36:37] op_sel:[1,0] op_sel_hi:[0,1] neg_lo:[0,1] neg_hi:[0,1]
	v_pk_fma_f32 v[96:97], v[96:97], v[96:97], s[26:27] neg_lo:[1,0,0] neg_hi:[1,0,0]
	v_pk_fma_f32 v[98:99], v[98:99], v[98:99], s[26:27] neg_lo:[1,0,0] neg_hi:[1,0,0]
	v_pk_fma_f32 v[100:101], v[100:101], v[100:101], s[24:25] neg_lo:[1,0,0] neg_hi:[1,0,0]
	v_pk_fma_f32 v[102:103], v[102:103], v[102:103], s[24:25] neg_lo:[1,0,0] neg_hi:[1,0,0]
	v_exp_f32_e32 v96, v96
	v_exp_f32_e32 v97, v97
	v_exp_f32_e32 v98, v98
	v_exp_f32_e32 v99, v99
	v_exp_f32_e32 v100, v100
	v_exp_f32_e32 v101, v101
	v_exp_f32_e32 v102, v102
	v_exp_f32_e32 v103, v103
	v_pk_add_f32 v[80:81], v[80:81], v[104:105]
	v_pk_fma_f32 v[84:85], v[104:105], v[42:43], v[84:85]
	v_pk_add_f32 v[88:89], v[88:89], v[104:105]
	v_pk_fma_f32 v[92:93], v[104:105], v[34:35], v[92:93]
	v_pk_add_f32 v[80:81], v[80:81], v[106:107]
	v_pk_fma_f32 v[84:85], v[106:107], v[44:45], v[84:85]
	v_pk_add_f32 v[90:91], v[90:91], v[106:107]
	v_pk_fma_f32 v[94:95], v[106:107], v[34:35], v[94:95]
	v_pk_add_f32 v[82:83], v[82:83], v[108:109]
	v_pk_fma_f32 v[86:87], v[108:109], v[42:43], v[86:87]
	v_pk_add_f32 v[88:89], v[88:89], v[108:109]
	v_pk_fma_f32 v[92:93], v[108:109], v[36:37], v[92:93]
	v_pk_add_f32 v[82:83], v[82:83], v[110:111]
	v_pk_fma_f32 v[86:87], v[110:111], v[44:45], v[86:87]
	v_pk_add_f32 v[90:91], v[90:91], v[110:111]
	v_pk_fma_f32 v[94:95], v[110:111], v[36:37], v[94:95]
	v_pk_add_f32 v[104:105], v[42:43], v[40:41] neg_lo:[0,1] neg_hi:[0,1]
	v_pk_add_f32 v[106:107], v[44:45], v[42:43] neg_lo:[0,1] neg_hi:[0,1]
	v_pk_add_f32 v[108:109], v[46:47], v[44:45] neg_lo:[0,1] neg_hi:[0,1]
	v_pk_fma_f32 v[104:105], v[104:105], v[104:105], s[22:23] neg_lo:[1,0,0] neg_hi:[1,0,0]
	v_pk_fma_f32 v[106:107], v[106:107], v[106:107], s[22:23] neg_lo:[1,0,0] neg_hi:[1,0,0]
	v_pk_fma_f32 v[108:109], v[108:109], v[108:109], s[22:23] neg_lo:[1,0,0] neg_hi:[1,0,0]
	v_exp_f32_e32 v104, v104
	v_exp_f32_e32 v105, v105
	v_exp_f32_e32 v106, v106
	v_exp_f32_e32 v107, v107
	v_exp_f32_e32 v108, v108
	v_exp_f32_e32 v109, v109
	v_pk_add_f32 v[82:83], v[82:83], v[96:97]
	v_pk_fma_f32 v[86:87], v[96:97], v[46:47], v[86:87]
	v_pk_add_f32 v[90:91], v[90:91], v[98:99]
	v_pk_fma_f32 v[94:95], v[98:99], v[38:39], v[94:95]
	v_pk_add_f32 v[80:81], v[80:81], v[100:101]
	v_pk_fma_f32 v[84:85], v[100:101], v[42:43], v[84:85] op_sel:[0,1,0] op_sel_hi:[1,0,1]
	v_pk_add_f32 v[88:89], v[88:89], v[100:101] op_sel:[0,1] op_sel_hi:[1,0]
	v_pk_fma_f32 v[92:93], v[100:101], v[34:35], v[92:93] op_sel:[1,1,0] op_sel_hi:[0,0,1]
	v_pk_add_f32 v[82:83], v[82:83], v[102:103]
	v_pk_fma_f32 v[86:87], v[102:103], v[44:45], v[86:87] op_sel:[0,1,0] op_sel_hi:[1,0,1]
	v_pk_add_f32 v[90:91], v[90:91], v[102:103] op_sel:[0,1] op_sel_hi:[1,0]
	v_pk_fma_f32 v[94:95], v[102:103], v[36:37], v[94:95] op_sel:[1,1,0] op_sel_hi:[0,0,1]
	v_sub_f32_e32 v96, v42, v25
	v_sub_f32_e32 v98, v41, v26
	v_sub_f32_e32 v100, v44, v27
	v_sub_f32_e32 v102, v43, v28
	v_sub_f32_e32 v97, v46, v29
	v_sub_f32_e32 v99, v45, v30
	v_sub_f32_e32 v101, v42, v33
	v_sub_f32_e32 v103, v41, v34
	v_fma_f32 v96, -v96, v96, s26
	v_fma_f32 v98, -v98, v98, s26
	v_fma_f32 v100, -v100, v100, s26
	v_fma_f32 v102, -v102, v102, s26
	v_fma_f32 v97, -v97, v97, s26
	v_fma_f32 v99, -v99, v99, s26
	v_fma_f32 v101, -v101, v101, s24
	v_fma_f32 v103, -v103, v103, s24
	v_exp_f32_e32 v96, v96
	v_exp_f32_e32 v98, v98
	v_exp_f32_e32 v100, v100
	v_exp_f32_e32 v102, v102
	v_exp_f32_e32 v97, v97
	v_exp_f32_e32 v99, v99
	v_exp_f32_e32 v101, v101
	v_exp_f32_e32 v103, v103
	v_pk_add_f32 v[88:89], v[88:89], v[104:105]
	v_pk_fma_f32 v[92:93], v[104:105], v[40:41], v[92:93]
	v_pk_add_f32 v[90:91], v[90:91], v[106:107]
	v_pk_add_f32 v[88:89], v[88:89], v[106:107]
	v_pk_fma_f32 v[92:93], v[106:107], v[44:45], v[92:93]
	v_pk_fma_f32 v[94:95], v[106:107], v[42:43], v[94:95]
	v_pk_add_f32 v[90:91], v[90:91], v[108:109]
	v_pk_fma_f32 v[94:95], v[108:109], v[46:47], v[94:95]
	v_sub_f32_e32 v108, v44, v35
	v_sub_f32_e32 v110, v43, v36
	v_sub_f32_e32 v105, v46, v37
	v_sub_f32_e32 v107, v45, v38
	v_sub_f32_e32 v109, v42, v41
	v_sub_f32_e32 v104, v43, v42
	v_sub_f32_e32 v111, v44, v43
	v_sub_f32_e32 v106, v45, v44
	v_fma_f32 v108, -v108, v108, s24
	v_fma_f32 v110, -v110, v110, s24
	v_fma_f32 v105, -v105, v105, s24
	v_fma_f32 v107, -v107, v107, s24
	v_fma_f32 v109, -v109, v109, s20
	v_fma_f32 v104, -v104, v104, s20
	v_fma_f32 v111, -v111, v111, s20
	v_fma_f32 v106, -v106, v106, s20
	v_exp_f32_e32 v108, v108
	v_exp_f32_e32 v110, v110
	v_exp_f32_e32 v105, v105
	v_exp_f32_e32 v107, v107
	v_exp_f32_e32 v109, v109
	v_exp_f32_e32 v104, v104
	v_exp_f32_e32 v111, v111
	v_exp_f32_e32 v106, v106
	v_add_f32_e32 v88, v88, v96
	v_fmac_f32_e32 v92, v96, v25
	v_add_f32_e32 v72, v72, v98
	v_fmac_f32_e32 v76, v98, v41
	v_add_f32_e32 v73, v73, v100
	v_fmac_f32_e32 v77, v100, v44
	v_add_f32_e32 v90, v90, v100
	v_fmac_f32_e32 v94, v100, v27
	v_add_f32_e32 v74, v74, v102
	v_fmac_f32_e32 v78, v102, v43
	v_add_f32_e32 v89, v89, v102
	v_fmac_f32_e32 v93, v102, v28
	v_add_f32_e32 v75, v75, v97
	v_fmac_f32_e32 v79, v97, v46
	v_add_f32_e32 v91, v91, v99
	v_fmac_f32_e32 v95, v99, v30
	v_add_f32_e32 v88, v88, v101
	v_fmac_f32_e32 v92, v101, v33
	v_add_f32_e32 v80, v80, v103
	v_fmac_f32_e32 v84, v103, v41
	v_sub_f32_e64 v96, v46, v45
	v_fma_f32 v96, -v96, v96, s20
	s_nop 0
	v_exp_f32_e32 v96, v96
	v_add_f32_e32 v81, v81, v108
	v_fmac_f32_e32 v85, v108, v44
	v_add_f32_e32 v90, v90, v108
	v_fmac_f32_e32 v94, v108, v35
	v_add_f32_e32 v82, v82, v110
	v_fmac_f32_e32 v86, v110, v43
	v_add_f32_e32 v89, v89, v110
	v_fmac_f32_e32 v93, v110, v36
	v_add_f32_e32 v83, v83, v105
	v_fmac_f32_e32 v87, v105, v46
	v_add_f32_e32 v91, v91, v107
	v_fmac_f32_e32 v95, v107, v38
	v_add_f32_e32 v88, v88, v109
	v_fmac_f32_e32 v92, v109, v41
	v_add_f32_e32 v89, v89, v111
	v_fmac_f32_e32 v93, v111, v44
	v_add_f32_e32 v90, v90, v111
	v_fmac_f32_e32 v94, v111, v43
	v_pk_add_f32 v[88:89], v[88:89], v[104:105] op_sel_hi:[1,0]
	v_pk_fma_f32 v[92:93], v[104:105], v[42:43], v[92:93] op_sel:[0,1,0] op_sel_hi:[0,0,1]
	v_pk_add_f32 v[90:91], v[90:91], v[106:107] op_sel_hi:[1,0]
	v_pk_fma_f32 v[94:95], v[106:107], v[44:45], v[94:95] op_sel:[0,1,0] op_sel_hi:[0,0,1]
	s_nop 0
	v_add_f32_e32 v91, v91, v96
	v_fmac_f32_e32 v95, v96, v46
	v_rcp_f32_e32 v96, v72
	v_rcp_f32_e32 v97, v73
	v_rcp_f32_e32 v98, v74
	v_rcp_f32_e64 v99, v75
	v_pk_mul_f32 v[76:77], v[76:77], s[34:35]
	v_pk_mul_f32 v[78:79], v[78:79], s[34:35]
	v_pk_mul_f32 v[76:77], v[76:77], v[96:97]
	v_pk_mul_f32 v[78:79], v[78:79], v[98:99]
	s_nop 0
	s_nop 0
	buffer_store_dwordx4 v[76:79], v114, s[12:15], 0 offen offset:2048 sc1
	s_waitcnt vmcnt(5)
	s_nop 0
	v_mov_b32_dpp v48, v52 row_shr:1 row_mask:0xf bank_mask:0xf
	v_mov_b32_dpp v49, v53 row_shr:1 row_mask:0xf bank_mask:0xf
	v_mov_b32_dpp v54, v50 row_shl:1 row_mask:0xf bank_mask:0xf
	v_mov_b32_dpp v55, v51 row_shl:1 row_mask:0xf bank_mask:0xf
	v_pk_mul_f32 v[50:51], v[50:51], s[32:33]
	v_pk_mul_f32 v[52:53], v[52:53], s[32:33]
	v_cndmask_b32_e64 v49, v49, v48, vcc
	v_cndmask_b32_e64 v54, v54, v55, s[16:17]
	v_pk_mul_f32 v[48:49], v[48:49], s[32:33]
	v_pk_mul_f32 v[54:55], v[54:55], s[32:33]
	s_setprio 0
	s_nop 0
	v_pk_add_f32 v[96:97], v[48:49], v[34:35] neg_lo:[0,1] neg_hi:[0,1]
	v_pk_add_f32 v[98:99], v[50:51], v[34:35] neg_lo:[0,1] neg_hi:[0,1]
	v_pk_add_f32 v[100:101], v[52:53], v[34:35] neg_lo:[0,1] neg_hi:[0,1]
	v_pk_add_f32 v[102:103], v[50:51], v[36:37] neg_lo:[0,1] neg_hi:[0,1]
	v_pk_fma_f32 v[96:97], v[96:97], v[96:97], s[28:29] neg_lo:[1,0,0] neg_hi:[1,0,0]
	v_pk_fma_f32 v[98:99], v[98:99], v[98:99], s[22:23] neg_lo:[1,0,0] neg_hi:[1,0,0]
	v_pk_fma_f32 v[100:101], v[100:101], v[100:101], s[28:29] neg_lo:[1,0,0] neg_hi:[1,0,0]
	v_pk_fma_f32 v[102:103], v[102:103], v[102:103], s[28:29] neg_lo:[1,0,0] neg_hi:[1,0,0]
	v_exp_f32_e32 v96, v96
	v_exp_f32_e32 v97, v97
	v_exp_f32_e32 v98, v98
	v_exp_f32_e32 v99, v99
	v_exp_f32_e32 v100, v100
	v_exp_f32_e32 v101, v101
	v_exp_f32_e32 v102, v102
	v_exp_f32_e32 v103, v103
	v_pk_add_f32 v[104:105], v[52:53], v[36:37] neg_lo:[0,1] neg_hi:[0,1]
	v_pk_add_f32 v[106:107], v[54:55], v[36:37] neg_lo:[0,1] neg_hi:[0,1]
	v_pk_add_f32 v[108:109], v[50:51], v[34:35] op_sel:[1,0] op_sel_hi:[0,1] neg_lo:[0,1] neg_hi:[0,1]
	v_pk_add_f32 v[110:111], v[52:53], v[36:37] op_sel:[1,0] op_sel_hi:[0,1] neg_lo:[0,1] neg_hi:[0,1]
	v_pk_fma_f32 v[104:105], v[104:105], v[104:105], s[22:23] neg_lo:[1,0,0] neg_hi:[1,0,0]
	v_pk_fma_f32 v[106:107], v[106:107], v[106:107], s[28:29] neg_lo:[1,0,0] neg_hi:[1,0,0]
	v_pk_fma_f32 v[108:109], v[108:109], v[108:109], s[26:27] neg_lo:[1,0,0] neg_hi:[1,0,0]
	v_pk_fma_f32 v[110:111], v[110:111], v[110:111], s[26:27] neg_lo:[1,0,0] neg_hi:[1,0,0]
	v_exp_f32_e32 v104, v104
	v_exp_f32_e32 v105, v105
	v_exp_f32_e32 v106, v106
	v_exp_f32_e32 v107, v107
	v_exp_f32_e32 v108, v108
	v_exp_f32_e32 v109, v109
	v_exp_f32_e32 v110, v110
	v_exp_f32_e32 v111, v111
	v_pk_add_f32 v[80:81], v[80:81], v[96:97]
	v_pk_fma_f32 v[84:85], v[96:97], v[48:49], v[84:85]
	v_pk_add_f32 v[82:83], v[82:83], v[102:103]
	v_pk_add_f32 v[80:81], v[80:81], v[98:99]
	v_pk_fma_f32 v[84:85], v[98:99], v[50:51], v[84:85]
	v_pk_fma_f32 v[86:87], v[102:103], v[50:51], v[86:87]
	v_pk_add_f32 v[80:81], v[80:81], v[100:101]
	v_pk_fma_f32 v[84:85], v[100:101], v[52:53], v[84:85]
	v_pk_add_f32 v[96:97], v[48:49], v[42:43] neg_lo:[0,1] neg_hi:[0,1]
	v_pk_add_f32 v[98:99], v[50:51], v[42:43] neg_lo:[0,1] neg_hi:[0,1]
	v_pk_add_f32 v[100:101], v[52:53], v[42:43] neg_lo:[0,1] neg_hi:[0,1]
	v_pk_add_f32 v[102:103], v[50:51], v[44:45] neg_lo:[0,1] neg_hi:[0,1]
	v_pk_fma_f32 v[96:97], v[96:97], v[96:97], s[26:27] neg_lo:[1,0,0] neg_hi:[1,0,0]
	v_pk_fma_f32 v[98:99], v[98:99], v[98:99], s[20:21] neg_lo:[1,0,0] neg_hi:[1,0,0]
	v_pk_fma_f32 v[100:101], v[100:101], v[100:101], s[26:27] neg_lo:[1,0,0] neg_hi:[1,0,0]
	v_pk_fma_f32 v[102:103], v[102:103], v[102:103], s[26:27] neg_lo:[1,0,0] neg_hi:[1,0,0]
	v_exp_f32_e32 v96, v96
	v_exp_f32_e32 v97, v97
	v_exp_f32_e32 v98, v98
	v_exp_f32_e32 v99, v99
	v_exp_f32_e32 v100, v100
	v_exp_f32_e32 v101, v101
	v_exp_f32_e32 v102, v102
	v_exp_f32_e32 v103, v103
	v_pk_add_f32 v[82:83], v[82:83], v[104:105]
	v_pk_fma_f32 v[86:87], v[104:105], v[52:53], v[86:87]
	v_pk_add_f32 v[80:81], v[80:81], v[108:109]
	v_pk_add_f32 v[82:83], v[82:83], v[106:107]
	v_pk_fma_f32 v[86:87], v[106:107], v[54:55], v[86:87]
	v_pk_fma_f32 v[84:85], v[108:109], v[50:51], v[84:85] op_sel:[0,1,0] op_sel_hi:[1,0,1]
	v_pk_add_f32 v[82:83], v[82:83], v[110:111]
	v_pk_fma_f32 v[86:87], v[110:111], v[52:53], v[86:87] op_sel:[0,1,0] op_sel_hi:[1,0,1]
	v_pk_add_f32 v[104:105], v[52:53], v[44:45] neg_lo:[0,1] neg_hi:[0,1]
	v_pk_add_f32 v[106:107], v[54:55], v[44:45] neg_lo:[0,1] neg_hi:[0,1]
	v_pk_add_f32 v[108:109], v[50:51], v[42:43] op_sel:[1,0] op_sel_hi:[0,1] neg_lo:[0,1] neg_hi:[0,1]
	v_pk_add_f32 v[110:111], v[52:53], v[44:45] op_sel:[1,0] op_sel_hi:[0,1] neg_lo:[0,1] neg_hi:[0,1]
	v_pk_fma_f32 v[104:105], v[104:105], v[104:105], s[20:21] neg_lo:[1,0,0] neg_hi:[1,0,0]
	v_pk_fma_f32 v[106:107], v[106:107], v[106:107], s[26:27] neg_lo:[1,0,0] neg_hi:[1,0,0]
	v_pk_fma_f32 v[108:109], v[108:109], v[108:109], s[24:25] neg_lo:[1,0,0] neg_hi:[1,0,0]
	v_pk_fma_f32 v[110:111], v[110:111], v[110:111], s[24:25] neg_lo:[1,0,0] neg_hi:[1,0,0]
	v_exp_f32_e32 v104, v104
	v_exp_f32_e32 v105, v105
	v_exp_f32_e32 v106, v106
	v_exp_f32_e32 v107, v107
	v_exp_f32_e32 v108, v108
	v_exp_f32_e32 v109, v109
	v_exp_f32_e32 v110, v110
	v_exp_f32_e32 v111, v111
	v_pk_add_f32 v[88:89], v[88:89], v[96:97]
	v_pk_fma_f32 v[92:93], v[96:97], v[48:49], v[92:93]
	v_pk_add_f32 v[90:91], v[90:91], v[102:103]
	v_pk_add_f32 v[88:89], v[88:89], v[98:99]
	v_pk_fma_f32 v[92:93], v[98:99], v[50:51], v[92:93]
	v_pk_fma_f32 v[94:95], v[102:103], v[50:51], v[94:95]
	v_pk_add_f32 v[88:89], v[88:89], v[100:101]
	v_pk_fma_f32 v[92:93], v[100:101], v[52:53], v[92:93]
	v_sub_f32_e32 v96, v49, v34
	v_sub_f32_e32 v98, v52, v35
	v_sub_f32_e32 v100, v51, v36
	v_sub_f32_e32 v102, v54, v37
	v_sub_f32_e32 v97, v49, v42
	v_sub_f32_e32 v99, v52, v43
	v_sub_f32_e32 v101, v51, v44
	v_sub_f32_e32 v103, v54, v45
	v_fma_f32 v96, -v96, v96, s26
	v_fma_f32 v98, -v98, v98, s26
	v_fma_f32 v100, -v100, v100, s26
	v_fma_f32 v102, -v102, v102, s26
	v_fma_f32 v97, -v97, v97, s24
	v_fma_f32 v99, -v99, v99, s24
	v_fma_f32 v101, -v101, v101, s24
	v_fma_f32 v103, -v103, v103, s24
	v_exp_f32_e32 v96, v96
	v_exp_f32_e32 v98, v98
	v_exp_f32_e32 v100, v100
	v_exp_f32_e32 v102, v102
	v_exp_f32_e32 v97, v97
	v_exp_f32_e32 v99, v99
	v_exp_f32_e32 v101, v101
	v_exp_f32_e32 v103, v103
	v_pk_add_f32 v[90:91], v[90:91], v[104:105]
	v_pk_fma_f32 v[94:95], v[104:105], v[52:53], v[94:95]
	v_pk_add_f32 v[88:89], v[88:89], v[108:109]
	v_pk_add_f32 v[90:91], v[90:91], v[106:107]
	v_pk_fma_f32 v[94:95], v[106:107], v[54:55], v[94:95]
	v_pk_fma_f32 v[92:93], v[108:109], v[50:51], v[92:93] op_sel:[0,1,0] op_sel_hi:[1,0,1]
	v_pk_add_f32 v[90:91], v[90:91], v[110:111]
	v_pk_fma_f32 v[94:95], v[110:111], v[52:53], v[94:95] op_sel:[0,1,0] op_sel_hi:[1,0,1]
	v_add_f32_e32 v80, v80, v96
	v_fmac_f32_e32 v84, v96, v49
	v_add_f32_e32 v81, v81, v98
	v_fmac_f32_e32 v85, v98, v52
	v_add_f32_e32 v82, v82, v100
	v_fmac_f32_e32 v86, v100, v51
	v_add_f32_e32 v83, v83, v102
	v_fmac_f32_e32 v87, v102, v54
	v_add_f32_e32 v88, v88, v97
	v_fmac_f32_e32 v92, v97, v49
	v_add_f32_e32 v89, v89, v99
	v_fmac_f32_e32 v93, v99, v52
	v_add_f32_e32 v90, v90, v101
	v_fmac_f32_e32 v94, v101, v51
	v_add_f32_e32 v91, v91, v103
	v_fmac_f32_e32 v95, v103, v54
	v_rcp_f32_e32 v96, v80
	v_rcp_f32_e32 v97, v81
	v_rcp_f32_e32 v98, v82
	v_rcp_f32_e32 v99, v83
	v_pk_mul_f32 v[84:85], v[84:85], s[34:35]
	v_pk_mul_f32 v[86:87], v[86:87], s[34:35]
	v_pk_mul_f32 v[84:85], v[84:85], v[96:97]
	v_pk_mul_f32 v[86:87], v[86:87], v[98:99]
	s_nop 0
	s_nop 0
	buffer_store_dwordx4 v[84:87], v119, s[12:15], 0 offen sc1
	s_waitcnt vmcnt(3)
	s_nop 0
	v_mov_b32_dpp v56, v60 row_shr:1 row_mask:0xf bank_mask:0xf
	v_mov_b32_dpp v57, v61 row_shr:1 row_mask:0xf bank_mask:0xf
	v_mov_b32_dpp v62, v58 row_shl:1 row_mask:0xf bank_mask:0xf
	v_mov_b32_dpp v63, v59 row_shl:1 row_mask:0xf bank_mask:0xf
	v_pk_mul_f32 v[58:59], v[58:59], s[32:33]
	v_pk_mul_f32 v[60:61], v[60:61], s[32:33]
	v_cndmask_b32_e64 v57, v57, v56, vcc
	v_cndmask_b32_e64 v62, v62, v63, s[16:17]
	v_pk_mul_f32 v[56:57], v[56:57], s[32:33]
	v_pk_mul_f32 v[62:63], v[62:63], s[32:33]
	s_setprio 0
	s_nop 0
	v_pk_add_f32 v[96:97], v[56:57], v[42:43] neg_lo:[0,1] neg_hi:[0,1]
	v_pk_add_f32 v[98:99], v[58:59], v[42:43] neg_lo:[0,1] neg_hi:[0,1]
	v_pk_add_f32 v[100:101], v[60:61], v[42:43] neg_lo:[0,1] neg_hi:[0,1]
	v_pk_add_f32 v[102:103], v[58:59], v[44:45] neg_lo:[0,1] neg_hi:[0,1]
	v_pk_fma_f32 v[96:97], v[96:97], v[96:97], s[28:29] neg_lo:[1,0,0] neg_hi:[1,0,0]
	v_pk_fma_f32 v[98:99], v[98:99], v[98:99], s[22:23] neg_lo:[1,0,0] neg_hi:[1,0,0]
	v_pk_fma_f32 v[100:101], v[100:101], v[100:101], s[28:29] neg_lo:[1,0,0] neg_hi:[1,0,0]
	v_pk_fma_f32 v[102:103], v[102:103], v[102:103], s[28:29] neg_lo:[1,0,0] neg_hi:[1,0,0]
	v_exp_f32_e32 v96, v96
	v_exp_f32_e32 v97, v97
	v_exp_f32_e32 v98, v98
	v_exp_f32_e32 v99, v99
	v_exp_f32_e32 v100, v100
	v_exp_f32_e32 v101, v101
	v_exp_f32_e32 v102, v102
	v_exp_f32_e32 v103, v103
	v_pk_add_f32 v[104:105], v[60:61], v[44:45] neg_lo:[0,1] neg_hi:[0,1]
	v_pk_add_f32 v[106:107], v[62:63], v[44:45] neg_lo:[0,1] neg_hi:[0,1]
	v_pk_add_f32 v[108:109], v[58:59], v[42:43] op_sel:[1,0] op_sel_hi:[0,1] neg_lo:[0,1] neg_hi:[0,1]
	v_pk_add_f32 v[110:111], v[60:61], v[44:45] op_sel:[1,0] op_sel_hi:[0,1] neg_lo:[0,1] neg_hi:[0,1]
	v_pk_fma_f32 v[104:105], v[104:105], v[104:105], s[22:23] neg_lo:[1,0,0] neg_hi:[1,0,0]
	v_pk_fma_f32 v[106:107], v[106:107], v[106:107], s[28:29] neg_lo:[1,0,0] neg_hi:[1,0,0]
	v_pk_fma_f32 v[108:109], v[108:109], v[108:109], s[26:27] neg_lo:[1,0,0] neg_hi:[1,0,0]
	v_pk_fma_f32 v[110:111], v[110:111], v[110:111], s[26:27] neg_lo:[1,0,0] neg_hi:[1,0,0]
	v_exp_f32_e32 v104, v104
	v_exp_f32_e32 v105, v105
	v_exp_f32_e32 v106, v106
	v_exp_f32_e32 v107, v107
	v_exp_f32_e32 v108, v108
	v_exp_f32_e32 v109, v109
	v_exp_f32_e32 v110, v110
	v_exp_f32_e32 v111, v111
	v_pk_add_f32 v[88:89], v[88:89], v[96:97]
	v_pk_fma_f32 v[92:93], v[96:97], v[56:57], v[92:93]
	v_pk_add_f32 v[90:91], v[90:91], v[102:103]
	v_pk_add_f32 v[88:89], v[88:89], v[98:99]
	v_pk_fma_f32 v[92:93], v[98:99], v[58:59], v[92:93]
	v_pk_fma_f32 v[94:95], v[102:103], v[58:59], v[94:95]
	v_pk_add_f32 v[88:89], v[88:89], v[100:101]
	v_pk_fma_f32 v[92:93], v[100:101], v[60:61], v[92:93]
	v_sub_f32_e32 v96, v57, v42
	v_sub_f32_e32 v98, v60, v43
	v_sub_f32_e32 v100, v59, v44
	v_sub_f32_e32 v102, v62, v45
	v_fma_f32 v96, -v96, v96, s26
	v_fma_f32 v98, -v98, v98, s26
	v_fma_f32 v100, -v100, v100, s26
	v_fma_f32 v102, -v102, v102, s26
	v_exp_f32_e32 v96, v96
	v_exp_f32_e32 v98, v98
	v_exp_f32_e32 v100, v100
	v_exp_f32_e32 v102, v102
	v_pk_add_f32 v[90:91], v[90:91], v[104:105]
	v_pk_fma_f32 v[94:95], v[104:105], v[60:61], v[94:95]
	v_pk_add_f32 v[88:89], v[88:89], v[108:109]
	v_pk_add_f32 v[90:91], v[90:91], v[106:107]
	v_pk_fma_f32 v[94:95], v[106:107], v[62:63], v[94:95]
	v_pk_fma_f32 v[92:93], v[108:109], v[58:59], v[92:93] op_sel:[0,1,0] op_sel_hi:[1,0,1]
	v_pk_add_f32 v[90:91], v[90:91], v[110:111]
	v_pk_fma_f32 v[94:95], v[110:111], v[60:61], v[94:95] op_sel:[0,1,0] op_sel_hi:[1,0,1]
	v_add_f32_e32 v88, v88, v96
	v_fmac_f32_e32 v92, v96, v57
	v_add_f32_e32 v89, v89, v98
	v_fmac_f32_e32 v93, v98, v60
	v_add_f32_e32 v90, v90, v100
	v_fmac_f32_e32 v94, v100, v59
	v_add_f32_e32 v91, v91, v102
	v_fmac_f32_e32 v95, v102, v62
	v_rcp_f32_e32 v96, v88
	v_rcp_f32_e32 v97, v89
	v_rcp_f32_e32 v98, v90
	v_rcp_f32_e32 v99, v91
	v_pk_mul_f32 v[92:93], v[92:93], s[34:35]
	v_pk_mul_f32 v[94:95], v[94:95], s[34:35]
	v_pk_mul_f32 v[92:93], v[92:93], v[96:97]
	v_pk_mul_f32 v[94:95], v[94:95], v[98:99]
	s_nop 0
	s_nop 0
	buffer_store_dwordx4 v[92:95], v119, s[12:15], 0 offen offset:2048 sc1
	s_endpgm
